# fragment build moved into last-block wait shadow; softmax exchanges via permlane swaps (baseline prologue kept)
# speedup vs baseline: 1.0092x; 1.0092x over previous
_Z12fused_kernelPKfS0_Pf:
	s_load_dwordx4 s[12:15], s[0:1], 0x0
	s_load_dwordx2 s[8:9], s[0:1], 0x10
	s_lshl_b32 s0, s2, 5
	s_and_b32 s0, s0, 0xe0
	s_lshr_b32 s3, s2, 3
	s_add_i32 s0, s0, s3
	v_and_b32_e32 v1, 63, v0
	v_lshrrev_b32_e32 v200, 6, v0
	s_lshl_b32 s0, s0, 17
	v_lshl_add_u32 v2, v200, 25, s0
	v_lshlrev_b32_e32 v198, 4, v1
	v_or_b32_e32 v203, v2, v198
	v_lshlrev_b32_e32 v196, 10, v200
	v_or_b32_e32 v233, v203, v196
	s_waitcnt lgkmcnt(0)
	s_and_b32 s5, s13, 0xffff
	s_mov_b32 s7, 0x20000
	s_brev_b32 s6, 8
	s_mov_b32 s4, s12
	v_or_b32_e32 v2, 0x2000, v233
	buffer_load_dwordx4 v[70:73], v233, s[4:7], 0 offen nt
	buffer_load_dwordx4 v[66:69], v2, s[4:7], 0 offen nt
	v_or_b32_e32 v2, 0x4000, v233
	v_or_b32_e32 v3, 0x6000, v233
	buffer_load_dwordx4 v[78:81], v2, s[4:7], 0 offen nt
	buffer_load_dwordx4 v[74:77], v3, s[4:7], 0 offen nt
	v_or_b32_e32 v2, 0x8000, v233
	v_lshlrev_b32_e32 v194, 4, v0
	v_mov_b32_e32 v195, 0
	s_movk_i32 s16, 0x2000
	v_or_b32_e32 v3, 0xa000, v233
	buffer_load_dwordx4 v[86:89], v2, s[4:7], 0 offen nt
	buffer_load_dwordx4 v[82:85], v3, s[4:7], 0 offen nt
	v_or_b32_e32 v2, 0xc000, v233
	v_lshl_add_u64 v[106:107], s[14:15], 0, v[194:195]
	v_or_b32_e32 v3, 0xe000, v233
	buffer_load_dwordx4 v[94:97], v2, s[4:7], 0 offen nt
	buffer_load_dwordx4 v[90:93], v3, s[4:7], 0 offen nt
	global_load_dwordx4 v[102:105], v194, s[14:15]
	v_add_co_u32_e32 v2, vcc, s16, v106
	v_lshrrev_b32_e32 v110, 3, v0
	s_nop 0
	v_addc_co_u32_e32 v3, vcc, 0, v107, vcc
	global_load_dwordx4 v[98:101], v[2:3], off
	v_bfe_u32 v111, v0, 1, 2
	v_lshlrev_b32_e32 v108, 3, v0
	v_lshlrev_b32_e32 v199, 8, v110
	v_and_b32_e32 v109, 8, v108
	v_lshlrev_b32_e32 v110, 10, v110
	v_lshlrev_b32_e32 v112, 8, v111
	s_mov_b32 s25, 0x26000
	v_or3_b32 v110, v112, v110, v109
	v_add_co_u32_e32 v112, vcc, s25, v106
	s_movk_i32 s17, 0x4000
	s_nop 0
	v_addc_co_u32_e32 v113, vcc, 0, v107, vcc
	s_waitcnt vmcnt(1)
	v_cvt_pk_bf16_f32 v144, v102, v103
	s_movk_i32 s11, 0x6000
	s_mov_b32 s13, 0x8000
	v_or_b32_e32 v4, 0x10000, v233
	v_or_b32_e32 v2, 0x12000, v233
	s_mov_b32 s10, 0xa000
	buffer_load_dwordx4 v[150:153], v4, s[4:7], 0 offen nt
	buffer_load_dwordx4 v[146:149], v2, s[4:7], 0 offen nt
	v_or_b32_e32 v2, 0x14000, v233
	v_or_b32_e32 v3, 0x16000, v233
	buffer_load_dwordx4 v[162:165], v2, s[4:7], 0 offen nt
	buffer_load_dwordx4 v[154:157], v3, s[4:7], 0 offen nt
	v_or_b32_e32 v2, 0x18000, v233
	s_mov_b32 s12, 0xc000
	v_or_b32_e32 v3, 0x1a000, v233
	buffer_load_dwordx4 v[174:177], v2, s[4:7], 0 offen nt
	buffer_load_dwordx4 v[166:169], v3, s[4:7], 0 offen nt
	v_or_b32_e32 v2, 0x1c000, v233
	v_or_b32_e32 v3, 0x1e000, v233
	buffer_load_dwordx4 v[182:185], v2, s[4:7], 0 offen nt
	buffer_load_dwordx4 v[178:181], v3, s[4:7], 0 offen nt
	v_add_u32_e32 v2, 0x400, v196
	s_movk_i32 s0, 0x1c00
	s_mov_b32 s1, 0xe000
	v_and_or_b32 v2, v2, s0, v203
	v_or_b32_e32 v3, 0x2000, v2
	s_mov_b32 s18, 0x10000
	buffer_load_dwordx4 v[62:65], v2, s[4:7], 0 offen nt
	buffer_load_dwordx4 v[38:41], v3, s[4:7], 0 offen nt
	v_or_b32_e32 v3, 0x4000, v2
	v_or_b32_e32 v4, 0x6000, v2
	buffer_load_dwordx4 v[42:45], v3, s[4:7], 0 offen nt
	buffer_load_dwordx4 v[14:17], v4, s[4:7], 0 offen nt
	v_or_b32_e32 v3, 0x8000, v2
	s_mov_b32 s23, 0x12000
	v_or_b32_e32 v4, 0xa000, v2
	buffer_load_dwordx4 v[46:49], v3, s[4:7], 0 offen nt
	buffer_load_dwordx4 v[18:21], v4, s[4:7], 0 offen nt
	v_or_b32_e32 v3, 0xc000, v2
	v_or_b32_e32 v4, 0xe000, v2
	buffer_load_dwordx4 v[50:53], v3, s[4:7], 0 offen nt
	buffer_load_dwordx4 v[22:25], v4, s[4:7], 0 offen nt
	v_or_b32_e32 v3, 0x10000, v2
	s_mov_b32 s22, 0x14000
	v_or_b32_e32 v4, 0x12000, v2
	buffer_load_dwordx4 v[54:57], v3, s[4:7], 0 offen nt
	buffer_load_dwordx4 v[26:29], v4, s[4:7], 0 offen nt
	v_or_b32_e32 v3, 0x14000, v2
	v_or_b32_e32 v4, 0x16000, v2
	buffer_load_dwordx4 v[58:61], v3, s[4:7], 0 offen nt
	buffer_load_dwordx4 v[30:33], v4, s[4:7], 0 offen nt
	v_or_b32_e32 v3, 0x18000, v2
	s_mov_b32 s21, 0x16000
	v_or_b32_e32 v4, 0x1a000, v2
	buffer_load_dwordx4 v[34:37], v3, s[4:7], 0 offen nt
	buffer_load_dwordx4 v[6:9], v4, s[4:7], 0 offen nt
	v_or_b32_e32 v3, 0x1c000, v2
	v_or_b32_e32 v2, 0x1e000, v2
	buffer_load_dwordx4 v[10:13], v3, s[4:7], 0 offen nt
	s_nop 0
	buffer_load_dwordx4 v[2:5], v2, s[4:7], 0 offen nt
	v_cvt_pk_bf16_f32 v145, v104, v105
	global_load_dwordx4 v[112:115], v[112:113], off
	s_mov_b32 s20, 0x18000
	s_mov_b32 s19, 0x1a000
	s_mov_b32 s15, 0x1c000
	s_mov_b32 s14, 0x1e000
	s_mov_b32 s25, 0x22000
	v_bfe_u32 v201, v0, 4, 2
	s_mov_b32 s26, 0x3e13bb63
	v_lshlrev_b32_e32 v202, 2, v201
	v_cvt_pk_bf16_f32 v66, v66, v67
	v_cvt_pk_bf16_f32 v67, v68, v69
	v_pk_add_f32 v[116:117], v[102:103], 0 op_sel_hi:[1,0]
	v_add_co_u32_e32 v102, vcc, s17, v106
	v_pk_add_f32 v[118:119], v[104:105], 0 op_sel_hi:[1,0]
	s_nop 0
	v_addc_co_u32_e32 v103, vcc, 0, v107, vcc
	s_waitcnt vmcnt(25)
	v_pk_add_f32 v[224:225], v[116:117], v[98:99]
	v_add_co_u32_e32 v116, vcc, s11, v106
	global_load_dwordx4 v[102:105], v[102:103], off
	s_nop 0
	v_addc_co_u32_e32 v117, vcc, 0, v107, vcc
	v_add_co_u32_e32 v120, vcc, s13, v106
	v_pk_add_f32 v[226:227], v[118:119], v[100:101]
	s_nop 0
	v_addc_co_u32_e32 v121, vcc, 0, v107, vcc
	v_add_co_u32_e32 v124, vcc, s10, v106
	global_load_dwordx4 v[116:119], v[116:117], off
	s_nop 0
	global_load_dwordx4 v[120:123], v[120:121], off
	v_addc_co_u32_e32 v125, vcc, 0, v107, vcc
	v_add_co_u32_e32 v128, vcc, s12, v106
	global_load_dwordx4 v[124:127], v[124:125], off
	s_nop 0
	v_addc_co_u32_e32 v129, vcc, 0, v107, vcc
	v_add_co_u32_e32 v132, vcc, s1, v106
	global_load_dwordx4 v[128:131], v[128:129], off
	s_nop 0
	v_addc_co_u32_e32 v133, vcc, 0, v107, vcc
	v_add_co_u32_e32 v136, vcc, s18, v106
	global_load_dwordx4 v[132:135], v[132:133], off
	s_nop 0
	v_addc_co_u32_e32 v137, vcc, 0, v107, vcc
	v_add_co_u32_e32 v140, vcc, s23, v106
	global_load_dwordx4 v[136:139], v[136:137], off
	s_nop 0
	v_addc_co_u32_e32 v141, vcc, 0, v107, vcc
	v_add_co_u32_e32 v158, vcc, s22, v106
	global_load_dwordx4 v[140:143], v[140:141], off
	s_nop 0
	v_addc_co_u32_e32 v159, vcc, 0, v107, vcc
	v_add_co_u32_e32 v170, vcc, s21, v106
	global_load_dwordx4 v[158:161], v[158:159], off
	s_nop 0
	v_addc_co_u32_e32 v171, vcc, 0, v107, vcc
	v_add_co_u32_e32 v186, vcc, s20, v106
	v_cvt_pk_bf16_f32 v98, v98, v99
	v_cvt_pk_bf16_f32 v99, v100, v101
	s_movk_i32 s24, 0xe0
	s_nop 0
	v_addc_co_u32_e32 v187, vcc, 0, v107, vcc
	v_add_co_u32_e32 v190, vcc, s19, v106
	global_load_dwordx4 v[170:173], v[170:171], off
	s_nop 0
	global_load_dwordx4 v[186:189], v[186:187], off
	v_addc_co_u32_e32 v191, vcc, 0, v107, vcc
	v_add_co_u32_e32 v204, vcc, s15, v106
	v_and_b32_e32 v197, 15, v0
	s_nop 0
	v_addc_co_u32_e32 v205, vcc, 0, v107, vcc
	v_add_co_u32_e32 v208, vcc, s14, v106
	global_load_dwordx4 v[190:193], v[190:191], off
	s_nop 0
	global_load_dwordx4 v[204:207], v[204:205], off
	v_addc_co_u32_e32 v209, vcc, 0, v107, vcc
	v_add_co_u32_e32 v212, vcc, s7, v106
	global_load_dwordx4 v[208:211], v[208:209], off
	s_nop 0
	v_addc_co_u32_e32 v213, vcc, 0, v107, vcc
	v_add_co_u32_e32 v216, vcc, s25, v106
	s_mov_b32 s25, 0x24000
	s_nop 0
	v_addc_co_u32_e32 v217, vcc, 0, v107, vcc
	global_load_dwordx4 v[212:215], v[212:213], off
	v_add_co_u32_e32 v106, vcc, s25, v106
	global_load_dwordx4 v[216:219], v[216:217], off
	s_nop 0
	v_addc_co_u32_e32 v107, vcc, 0, v107, vcc
	global_load_dwordx4 v[220:223], v[106:107], off
	ds_write2_b64 v110, v[144:145], v[98:99] offset1:2
	s_waitcnt vmcnt(16)
	v_pk_add_f32 v[98:99], v[224:225], v[102:103]
	v_pk_add_f32 v[100:101], v[226:227], v[104:105]
	v_cvt_pk_bf16_f32 v102, v102, v103
	v_cvt_pk_bf16_f32 v103, v104, v105
	s_waitcnt vmcnt(15)
	v_cvt_pk_bf16_f32 v104, v116, v117
	v_pk_add_f32 v[98:99], v[98:99], v[116:117]
	v_pk_add_f32 v[100:101], v[100:101], v[118:119]
	s_waitcnt vmcnt(14)
	v_pk_add_f32 v[98:99], v[98:99], v[120:121]
	v_pk_add_f32 v[100:101], v[100:101], v[122:123]
	v_cvt_pk_bf16_f32 v105, v118, v119
	s_waitcnt vmcnt(13)
	v_pk_add_f32 v[98:99], v[98:99], v[124:125]
	v_pk_add_f32 v[100:101], v[100:101], v[126:127]
	ds_write2_b64 v110, v[102:103], v[104:105] offset0:4 offset1:6
	v_cvt_pk_bf16_f32 v102, v120, v121
	v_cvt_pk_bf16_f32 v103, v122, v123
	s_waitcnt vmcnt(12)
	v_pk_add_f32 v[98:99], v[98:99], v[128:129]
	v_pk_add_f32 v[100:101], v[100:101], v[130:131]
	v_cvt_pk_bf16_f32 v104, v124, v125
	v_cvt_pk_bf16_f32 v105, v126, v127
	ds_write2_b64 v110, v[102:103], v[104:105] offset0:8 offset1:10
	s_waitcnt vmcnt(11)
	v_pk_add_f32 v[98:99], v[98:99], v[132:133]
	v_pk_add_f32 v[100:101], v[100:101], v[134:135]
	v_cvt_pk_bf16_f32 v102, v128, v129
	v_cvt_pk_bf16_f32 v103, v130, v131
	v_cvt_pk_bf16_f32 v104, v132, v133
	s_waitcnt vmcnt(10)
	v_pk_add_f32 v[98:99], v[98:99], v[136:137]
	v_pk_add_f32 v[100:101], v[100:101], v[138:139]
	v_cvt_pk_bf16_f32 v105, v134, v135
	ds_write2_b64 v110, v[102:103], v[104:105] offset0:12 offset1:14
	v_cvt_pk_bf16_f32 v102, v136, v137
	s_waitcnt vmcnt(9)
	v_pk_add_f32 v[98:99], v[98:99], v[140:141]
	v_pk_add_f32 v[100:101], v[100:101], v[142:143]
	v_cvt_pk_bf16_f32 v103, v138, v139
	v_cvt_pk_bf16_f32 v104, v140, v141
	v_cvt_pk_bf16_f32 v105, v142, v143
	s_waitcnt vmcnt(8)
	v_pk_add_f32 v[98:99], v[98:99], v[158:159]
	v_pk_add_f32 v[100:101], v[100:101], v[160:161]
	ds_write2_b64 v110, v[102:103], v[104:105] offset0:16 offset1:18
	v_lshlrev_b32_e32 v102, 6, v111
	v_or3_b32 v102, v199, v102, v109
	v_add_u32_e32 v106, 0xff00, v102
	v_cvt_pk_bf16_f32 v102, v158, v159
	v_cvt_pk_bf16_f32 v103, v160, v161
	s_waitcnt vmcnt(7)
	v_cvt_pk_bf16_f32 v104, v170, v171
	v_pk_add_f32 v[98:99], v[98:99], v[170:171]
	v_pk_add_f32 v[100:101], v[100:101], v[172:173]
	s_waitcnt vmcnt(6)
	v_pk_add_f32 v[98:99], v[98:99], v[186:187]
	v_pk_add_f32 v[100:101], v[100:101], v[188:189]
	v_cvt_pk_bf16_f32 v105, v172, v173
	ds_write2_b64 v110, v[102:103], v[104:105] offset0:20 offset1:22
	v_cvt_pk_bf16_f32 v102, v186, v187
	v_cvt_pk_bf16_f32 v103, v188, v189
	s_waitcnt vmcnt(5)
	v_cvt_pk_bf16_f32 v104, v190, v191
	v_pk_add_f32 v[98:99], v[98:99], v[190:191]
	v_pk_add_f32 v[100:101], v[100:101], v[192:193]
	s_waitcnt vmcnt(4)
	v_pk_add_f32 v[98:99], v[98:99], v[204:205]
	v_pk_add_f32 v[100:101], v[100:101], v[206:207]
	v_cvt_pk_bf16_f32 v105, v192, v193
	s_waitcnt vmcnt(3)
	v_pk_add_f32 v[98:99], v[98:99], v[208:209]
	v_pk_add_f32 v[100:101], v[100:101], v[210:211]
	ds_write2_b64 v110, v[102:103], v[104:105] offset0:24 offset1:26
	v_cvt_pk_bf16_f32 v102, v204, v205
	v_cvt_pk_bf16_f32 v103, v206, v207
	v_cvt_pk_bf16_f32 v104, v208, v209
	v_cvt_pk_bf16_f32 v105, v210, v211
	v_add_u32_e32 v107, 0x24800, v194
	s_waitcnt vmcnt(2)
	v_pk_add_f32 v[98:99], v[98:99], v[212:213]
	v_pk_add_f32 v[100:101], v[100:101], v[214:215]
	ds_write2_b64 v110, v[102:103], v[104:105] offset0:28 offset1:30
	s_waitcnt vmcnt(1)
	v_pk_add_f32 v[98:99], v[98:99], v[216:217]
	v_pk_add_f32 v[100:101], v[100:101], v[218:219]
	v_cvt_pk_bf16_f32 v102, v212, v213
	s_waitcnt vmcnt(0)
	v_pk_add_f32 v[98:99], v[98:99], v[220:221]
	v_pk_add_f32 v[100:101], v[100:101], v[222:223]
	v_pk_add_f32 v[98:99], v[98:99], v[112:113]
	v_pk_add_f32 v[100:101], v[100:101], v[114:115]
	v_cvt_pk_bf16_f32 v103, v214, v215
	v_cvt_pk_bf16_f32 v104, v216, v217
	v_cvt_pk_bf16_f32 v105, v218, v219
	v_pk_mul_f32 v[98:99], v[98:99], s[26:27] op_sel_hi:[1,0]
	v_pk_mul_f32 v[100:101], v[100:101], s[26:27] op_sel_hi:[1,0]
	ds_write2_b64 v106, v[102:103], v[104:105] offset0:32 offset1:34
	v_cvt_pk_bf16_f32 v102, v220, v221
	v_cvt_pk_bf16_f32 v103, v222, v223
	v_cvt_pk_bf16_f32 v104, v112, v113
	v_cvt_pk_bf16_f32 v105, v114, v115
	ds_write2_b64 v106, v[102:103], v[104:105] offset0:36 offset1:38
	ds_write_b128 v107, v[98:101]
	v_and_or_b32 v98, v0, 3, v202
	v_mov_b32_e32 v99, 0x10000
	v_lshl_or_b32 v204, v98, 4, v99
	s_movk_i32 s25, 0x2100
	v_mov_b32_e32 v98, 0x14000
	v_mad_u32_u24 v199, v200, s25, v98
	v_add_u32_e32 v98, 0x800, v196
	v_and_or_b32 v186, v98, s0, v203
	v_or_b32_e32 v98, 0x2000, v186
	s_waitcnt lgkmcnt(0)
	s_barrier
	buffer_load_dwordx4 v[102:105], v186, s[4:7], 0 offen nt
	s_nop 0
	buffer_load_dwordx4 v[98:101], v98, s[4:7], 0 offen nt
	v_or_b32_e32 v106, 0x4000, v186
	v_or_b32_e32 v107, 0x6000, v186
	v_or_b32_e32 v114, 0x8000, v186
	v_or_b32_e32 v115, 0xa000, v186
	v_or_b32_e32 v122, 0xc000, v186
	v_or_b32_e32 v123, 0xe000, v186
	v_or_b32_e32 v130, 0x10000, v186
	v_or_b32_e32 v131, 0x12000, v186
	v_or_b32_e32 v138, 0x14000, v186
	v_or_b32_e32 v139, 0x16000, v186
	v_or_b32_e32 v158, 0x18000, v186
	v_or_b32_e32 v159, 0x1a000, v186
	v_or_b32_e32 v187, 0x1c000, v186
	v_or_b32_e32 v186, 0x1e000, v186
	v_or_b32_e32 v213, v199, v109
	v_and_b32_e32 v214, 0x1f0, v108
	buffer_load_dwordx4 v[110:113], v106, s[4:7], 0 offen nt
	s_nop 0
	buffer_load_dwordx4 v[106:109], v107, s[4:7], 0 offen nt
	s_nop 0
	buffer_load_dwordx4 v[118:121], v114, s[4:7], 0 offen nt
	s_nop 0
	buffer_load_dwordx4 v[114:117], v115, s[4:7], 0 offen nt
	s_nop 0
	buffer_load_dwordx4 v[126:129], v122, s[4:7], 0 offen nt
	s_nop 0
	buffer_load_dwordx4 v[122:125], v123, s[4:7], 0 offen nt
	s_nop 0
	buffer_load_dwordx4 v[134:137], v130, s[4:7], 0 offen nt
	s_nop 0
	buffer_load_dwordx4 v[130:133], v131, s[4:7], 0 offen nt
	s_nop 0
	buffer_load_dwordx4 v[142:145], v138, s[4:7], 0 offen nt
	s_nop 0
	buffer_load_dwordx4 v[138:141], v139, s[4:7], 0 offen nt
	s_nop 0
	buffer_load_dwordx4 v[170:173], v158, s[4:7], 0 offen nt
	s_nop 0
	buffer_load_dwordx4 v[158:161], v159, s[4:7], 0 offen nt
	s_nop 0
	buffer_load_dwordx4 v[190:193], v187, s[4:7], 0 offen nt
	s_nop 0
	buffer_load_dwordx4 v[186:189], v186, s[4:7], 0 offen nt
	s_movk_i32 s25, 0x50
	v_xad_u32 v207, v214, s25, v213
	s_movk_i32 s25, 0x60
	v_xad_u32 v206, v214, s25, v213
	s_movk_i32 s25, 0x70
	v_xad_u32 v205, v214, s25, v213
	s_movk_i32 s25, 0x80
	v_xad_u32 v211, v214, 16, v213
	v_xad_u32 v231, v214, s25, v213
	s_movk_i32 s25, 0x90
	v_xad_u32 v210, v214, 32, v213
	v_xad_u32 v230, v214, s25, v213
	s_movk_i32 s25, 0xa0
	ds_write_b64 v211, v[66:67] offset:512
	v_cvt_pk_bf16_f32 v66, v78, v79
	v_cvt_pk_bf16_f32 v67, v80, v81
	v_xad_u32 v209, v214, 48, v213
	v_xad_u32 v229, v214, s25, v213
	s_movk_i32 s25, 0xb0
	ds_write_b64 v210, v[66:67] offset:1024
	v_cvt_pk_bf16_f32 v66, v74, v75
	v_cvt_pk_bf16_f32 v67, v76, v77
	v_xad_u32 v208, v214, 64, v213
	v_xad_u32 v228, v214, s25, v213
	s_movk_i32 s25, 0xc0
	ds_write_b64 v209, v[66:67] offset:1536
	v_cvt_pk_bf16_f32 v66, v86, v87
	v_cvt_pk_bf16_f32 v67, v88, v89
	v_xad_u32 v227, v214, s25, v213
	s_movk_i32 s25, 0xd0
	v_xad_u32 v225, v214, s24, v213
	s_movk_i32 s24, 0xf0
	ds_write_b64 v208, v[66:67] offset:2048
	v_cvt_pk_bf16_f32 v66, v82, v83
	v_cvt_pk_bf16_f32 v67, v84, v85
	v_add_u32_e32 v212, v213, v214
	v_xad_u32 v226, v214, s25, v213
	v_xad_u32 v224, v214, s24, v213
	v_lshl_add_u32 v213, v197, 9, v199
	v_bitop3_b32 v214, v201, v0, 15 bitop3:0x78
	ds_write_b64 v207, v[66:67] offset:2560
	v_cvt_pk_bf16_f32 v66, v94, v95
	v_cvt_pk_bf16_f32 v67, v96, v97
	v_lshl_or_b32 v223, v214, 4, v213
	v_bitop3_b32 v214, v201, v197, 4 bitop3:0x36
	ds_write_b64 v206, v[66:67] offset:3072
	v_cvt_pk_bf16_f32 v66, v90, v91
	v_cvt_pk_bf16_f32 v67, v92, v93
	v_lshl_or_b32 v222, v214, 4, v213
	v_bitop3_b32 v214, v201, v197, 8 bitop3:0x36
	ds_write_b64 v205, v[66:67] offset:3584
	v_cvt_pk_bf16_f32 v66, v150, v151
	v_cvt_pk_bf16_f32 v67, v152, v153
	v_lshl_or_b32 v221, v214, 4, v213
	v_bitop3_b32 v214, v201, v197, 12 bitop3:0x36
	ds_write_b64 v231, v[66:67] offset:4096
	v_cvt_pk_bf16_f32 v66, v146, v147
	v_cvt_pk_bf16_f32 v67, v148, v149
	v_lshl_or_b32 v219, v214, 4, v213
	v_bitop3_b32 v214, v201, v197, 16 bitop3:0x36
	ds_write_b64 v230, v[66:67] offset:4608
	v_cvt_pk_bf16_f32 v66, v162, v163
	v_cvt_pk_bf16_f32 v67, v164, v165
	v_lshl_add_u32 v218, v214, 4, v213
	v_bitop3_b32 v214, v201, v197, 20 bitop3:0x36
	ds_write_b64 v229, v[66:67] offset:5120
	v_cvt_pk_bf16_f32 v66, v154, v155
	v_cvt_pk_bf16_f32 v67, v156, v157
	v_lshl_add_u32 v217, v214, 4, v213
	v_bitop3_b32 v214, v201, v197, 24 bitop3:0x36
	ds_write_b64 v228, v[66:67] offset:5632
	v_cvt_pk_bf16_f32 v66, v174, v175
	v_cvt_pk_bf16_f32 v67, v176, v177
	v_lshl_add_u32 v216, v214, 4, v213
	v_bitop3_b32 v214, v201, v197, 28 bitop3:0x36
	ds_write_b64 v227, v[66:67] offset:6144
	v_cvt_pk_bf16_f32 v66, v166, v167
	v_cvt_pk_bf16_f32 v67, v168, v169
	v_add_u32_e32 v235, 3, v200
	v_lshl_add_u32 v213, v214, 4, v213
	ds_write_b64 v226, v[66:67] offset:6656
	v_cvt_pk_bf16_f32 v66, v182, v183
	v_cvt_pk_bf16_f32 v67, v184, v185
	v_cvt_pk_bf16_f32 v70, v70, v71
	v_cvt_pk_bf16_f32 v71, v72, v73
	ds_write_b64 v212, v[70:71]
	ds_write_b64 v225, v[66:67] offset:7168
	v_cvt_pk_bf16_f32 v66, v178, v179
	v_cvt_pk_bf16_f32 v67, v180, v181
	ds_write_b64 v224, v[66:67] offset:7680
	v_lshl_or_b32 v66, v200, 13, v198
	ds_read_b128 v[66:69], v66
	v_lshlrev_b32_e32 v220, 11, v200
	v_or_b32_e32 v70, v204, v220
	ds_read_b128 v[70:73], v70
	ds_read_b128 v[74:77], v223
	v_lshlrev_b32_e32 v232, 3, v200
	v_or_b32_e32 v214, 1, v232
	s_waitcnt lgkmcnt(0)
	v_mfma_f32_16x16x32_bf16 v[70:73], v[70:73], v[74:77], 0
	v_lshlrev_b32_e32 v215, 8, v214
	v_or_b32_e32 v78, v204, v215
	v_or_b32_e32 v184, 2, v232
	v_mfma_f32_16x16x32_bf16 v[66:69], v[66:69], v[74:77], 0
	v_lshl_or_b32 v74, v214, 10, v198
	ds_read_b128 v[74:77], v74
	ds_read_b128 v[78:81], v78
	ds_read_b128 v[82:85], v222
	v_lshlrev_b32_e32 v185, 8, v184
	s_waitcnt lgkmcnt(0)
	v_mfma_f32_16x16x32_bf16 v[70:73], v[78:81], v[82:85], v[70:73]
	v_or_b32_e32 v78, v204, v185
	v_or_b32_e32 v182, 3, v232
	v_lshlrev_b32_e32 v183, 8, v182
	v_mfma_f32_16x16x32_bf16 v[66:69], v[74:77], v[82:85], v[66:69]
	v_lshl_or_b32 v74, v184, 10, v198
	ds_read_b128 v[74:77], v74
	ds_read_b128 v[78:81], v78
	ds_read_b128 v[82:85], v221
	s_waitcnt lgkmcnt(0)
	v_mfma_f32_16x16x32_bf16 v[70:73], v[78:81], v[82:85], v[70:73]
	v_or_b32_e32 v78, v204, v183
	v_or_b32_e32 v180, 4, v232
	v_lshlrev_b32_e32 v181, 8, v180
	v_mfma_f32_16x16x32_bf16 v[66:69], v[74:77], v[82:85], v[66:69]
	v_lshl_or_b32 v74, v182, 10, v198
	ds_read_b128 v[74:77], v74
	ds_read_b128 v[78:81], v78
	ds_read_b128 v[82:85], v219
	s_waitcnt lgkmcnt(0)
	v_mfma_f32_16x16x32_bf16 v[66:69], v[74:77], v[82:85], v[66:69]
	v_lshl_or_b32 v74, v180, 10, v198
	ds_read_b128 v[74:77], v74
	v_or_b32_e32 v178, 5, v232
	v_mfma_f32_16x16x32_bf16 v[70:73], v[78:81], v[82:85], v[70:73]
	v_or_b32_e32 v78, v204, v181
	ds_read_b128 v[78:81], v78
	ds_read_b128 v[82:85], v218
	v_lshlrev_b32_e32 v179, 8, v178
	s_waitcnt lgkmcnt(0)
	v_mfma_f32_16x16x32_bf16 v[66:69], v[74:77], v[82:85], v[66:69]
	v_lshl_or_b32 v74, v178, 10, v198
	ds_read_b128 v[74:77], v74
	v_or_b32_e32 v176, 6, v232
	v_mfma_f32_16x16x32_bf16 v[70:73], v[78:81], v[82:85], v[70:73]
	v_or_b32_e32 v78, v204, v179
	ds_read_b128 v[78:81], v78
	ds_read_b128 v[82:85], v217
	v_lshlrev_b32_e32 v177, 8, v176
	s_waitcnt lgkmcnt(0)
	v_mfma_f32_16x16x32_bf16 v[66:69], v[74:77], v[82:85], v[66:69]
	v_lshl_or_b32 v74, v176, 10, v198
	ds_read_b128 v[74:77], v74
	v_or_b32_e32 v174, 7, v232
	v_mfma_f32_16x16x32_bf16 v[70:73], v[78:81], v[82:85], v[70:73]
	v_or_b32_e32 v78, v204, v177
	ds_read_b128 v[78:81], v78
	ds_read_b128 v[82:85], v216
	v_lshlrev_b32_e32 v175, 8, v174
	s_waitcnt lgkmcnt(0)
	v_mfma_f32_16x16x32_bf16 v[66:69], v[74:77], v[82:85], v[66:69]
	v_lshl_or_b32 v74, v174, 10, v198
	v_cvt_pk_bf16_f32 v14, v14, v15
	v_cvt_pk_bf16_f32 v15, v16, v17
	v_mfma_f32_16x16x32_bf16 v[70:73], v[78:81], v[82:85], v[70:73]
	v_or_b32_e32 v78, v204, v175
	ds_read_b128 v[74:77], v74
	ds_read_b128 v[78:81], v78
	ds_read_b128 v[82:85], v213
	ds_write_b64 v209, v[14:15] offset:1536
	v_cvt_pk_bf16_f32 v14, v46, v47
	v_cvt_pk_bf16_f32 v15, v48, v49
	ds_write_b64 v208, v[14:15] offset:2048
	v_cvt_pk_bf16_f32 v14, v18, v19
	v_cvt_pk_bf16_f32 v15, v20, v21
	ds_write_b64 v207, v[14:15] offset:2560
	v_cvt_pk_bf16_f32 v14, v50, v51
	v_cvt_pk_bf16_f32 v15, v52, v53
	ds_write_b64 v206, v[14:15] offset:3072
	v_cvt_pk_bf16_f32 v14, v22, v23
	v_cvt_pk_bf16_f32 v15, v24, v25
	ds_write_b64 v205, v[14:15] offset:3584
	v_cvt_pk_bf16_f32 v14, v54, v55
	v_cvt_pk_bf16_f32 v15, v56, v57
	v_cvt_pk_bf16_f32 v6, v6, v7
	v_cvt_pk_bf16_f32 v2, v2, v3
	ds_write_b64 v231, v[14:15] offset:4096
	v_cvt_pk_bf16_f32 v14, v26, v27
	v_cvt_pk_bf16_f32 v15, v28, v29
	v_cvt_pk_bf16_f32 v7, v8, v9
	ds_write_b64 v226, v[6:7] offset:6656
	v_cvt_pk_bf16_f32 v6, v10, v11
	v_cvt_pk_bf16_f32 v3, v4, v5
	ds_write_b64 v224, v[2:3] offset:7680
	v_lshlrev_b32_e32 v2, 10, v235
	ds_write_b64 v230, v[14:15] offset:4608
	v_cvt_pk_bf16_f32 v14, v58, v59
	v_cvt_pk_bf16_f32 v15, v60, v61
	v_cvt_pk_bf16_f32 v7, v12, v13
	ds_write_b64 v225, v[6:7] offset:7168
	v_and_or_b32 v6, v2, s0, v203
	ds_write_b64 v229, v[14:15] offset:5120
	v_cvt_pk_bf16_f32 v14, v30, v31
	v_cvt_pk_bf16_f32 v15, v32, v33
	v_or_b32_e32 v7, 0x2000, v6
	ds_write_b64 v228, v[14:15] offset:5632
	v_cvt_pk_bf16_f32 v14, v34, v35
	v_cvt_pk_bf16_f32 v15, v36, v37
	buffer_load_dwordx4 v[2:5], v6, s[4:7], 0 offen nt
	buffer_load_dwordx4 v[10:13], v7, s[4:7], 0 offen nt
	v_or_b32_e32 v7, 0x4000, v6
	ds_write_b64 v227, v[14:15] offset:6144
	buffer_load_dwordx4 v[14:17], v7, s[4:7], 0 offen nt
	v_or_b32_e32 v7, 0x6000, v6
	v_cvt_pk_bf16_f32 v38, v38, v39
	v_cvt_pk_bf16_f32 v39, v40, v41
	buffer_load_dwordx4 v[22:25], v7, s[4:7], 0 offen nt
	v_or_b32_e32 v7, 0x8000, v6
	ds_write_b64 v211, v[38:39] offset:512
	v_cvt_pk_bf16_f32 v38, v42, v43
	v_cvt_pk_bf16_f32 v39, v44, v45
	buffer_load_dwordx4 v[30:33], v7, s[4:7], 0 offen nt
	v_or_b32_e32 v7, 0xa000, v6
	ds_write_b64 v210, v[38:39] offset:1024
	buffer_load_dwordx4 v[38:41], v7, s[4:7], 0 offen nt
	v_or_b32_e32 v7, 0xc000, v6
	buffer_load_dwordx4 v[46:49], v7, s[4:7], 0 offen nt
	v_or_b32_e32 v7, 0xe000, v6
	v_cvt_pk_bf16_f32 v62, v62, v63
	v_cvt_pk_bf16_f32 v63, v64, v65
	buffer_load_dwordx4 v[54:57], v7, s[4:7], 0 offen nt
	v_or_b32_e32 v7, 0x10000, v6
	ds_write_b64 v212, v[62:63]
	buffer_load_dwordx4 v[62:65], v7, s[4:7], 0 offen nt
	v_or_b32_e32 v7, 0x12000, v6
	s_waitcnt lgkmcnt(14)
	v_mfma_f32_16x16x32_bf16 v[66:69], v[74:77], v[82:85], v[66:69]
	v_mfma_f32_16x16x32_bf16 v[74:77], v[78:81], v[82:85], v[70:73]
	s_nop 2
	buffer_load_dwordx4 v[70:73], v7, s[4:7], 0 offen nt
	v_or_b32_e32 v7, 0x14000, v6
	buffer_load_dwordx4 v[78:81], v7, s[4:7], 0 offen nt
	v_or_b32_e32 v7, 0x16000, v6
	buffer_load_dwordx4 v[86:89], v7, s[4:7], 0 offen nt
	v_or_b32_e32 v7, 0x18000, v6
	buffer_load_dwordx4 v[94:97], v7, s[4:7], 0 offen nt
	v_or_b32_e32 v7, 0x1a000, v6
	buffer_load_dwordx4 v[146:149], v7, s[4:7], 0 offen nt
	v_or_b32_e32 v7, 0x1c000, v6
	v_or_b32_e32 v6, 0x1e000, v6
	buffer_load_dwordx4 v[150:153], v7, s[4:7], 0 offen nt
	buffer_load_dwordx4 v[154:157], v6, s[4:7], 0 offen nt
	v_add_u32_e32 v6, 8, v232
	v_and_b32_e32 v50, 56, v6
	v_lshl_or_b32 v6, v50, 10, v198
	ds_read_b128 v[6:9], v6
	v_lshl_or_b32 v18, v50, 8, v204
	ds_read_b128 v[18:21], v18
	ds_read_b128 v[26:29], v223
	v_or_b32_e32 v34, 1, v50
	s_movk_i32 s24, 0x1000
	s_waitcnt lgkmcnt(0)
	v_mfma_f32_16x16x32_bf16 v[18:21], v[18:21], v[26:29], v[74:77]
	v_add_u32_e32 v234, 5, v200
	v_mfma_f32_16x16x32_bf16 v[6:9], v[6:9], v[26:29], v[66:69]
	v_lshl_or_b32 v26, v34, 10, v198
	ds_read_b128 v[26:29], v26
	v_lshl_or_b32 v34, v34, 8, v204
	ds_read_b128 v[34:37], v34
	ds_read_b128 v[42:45], v222
	s_waitcnt lgkmcnt(0)
	v_mfma_f32_16x16x32_bf16 v[18:21], v[34:37], v[42:45], v[18:21]
	v_or_b32_e32 v34, 2, v50
	v_mfma_f32_16x16x32_bf16 v[6:9], v[26:29], v[42:45], v[6:9]
	v_lshl_or_b32 v26, v34, 10, v198
	ds_read_b128 v[26:29], v26
	v_lshl_or_b32 v34, v34, 8, v204
	ds_read_b128 v[34:37], v34
	ds_read_b128 v[42:45], v221
	s_waitcnt lgkmcnt(0)
	v_mfma_f32_16x16x32_bf16 v[18:21], v[34:37], v[42:45], v[18:21]
	v_or_b32_e32 v34, 3, v50
	v_mfma_f32_16x16x32_bf16 v[6:9], v[26:29], v[42:45], v[6:9]
	v_lshl_or_b32 v26, v34, 10, v198
	ds_read_b128 v[26:29], v26
	v_lshl_or_b32 v34, v34, 8, v204
	ds_read_b128 v[34:37], v34
	ds_read_b128 v[42:45], v219
	s_waitcnt lgkmcnt(0)
	v_mfma_f32_16x16x32_bf16 v[18:21], v[34:37], v[42:45], v[18:21]
	v_or_b32_e32 v34, 4, v50
	v_mfma_f32_16x16x32_bf16 v[6:9], v[26:29], v[42:45], v[6:9]
	v_lshl_or_b32 v26, v34, 10, v198
	ds_read_b128 v[26:29], v26
	v_lshl_or_b32 v34, v34, 8, v204
	ds_read_b128 v[34:37], v34
	ds_read_b128 v[42:45], v218
	s_waitcnt lgkmcnt(0)
	v_mfma_f32_16x16x32_bf16 v[18:21], v[34:37], v[42:45], v[18:21]
	v_or_b32_e32 v34, 5, v50
	v_mfma_f32_16x16x32_bf16 v[6:9], v[26:29], v[42:45], v[6:9]
	v_lshl_or_b32 v26, v34, 10, v198
	ds_read_b128 v[26:29], v26
	v_lshl_or_b32 v34, v34, 8, v204
	ds_read_b128 v[34:37], v34
	ds_read_b128 v[42:45], v217
	s_waitcnt lgkmcnt(0)
	v_mfma_f32_16x16x32_bf16 v[18:21], v[34:37], v[42:45], v[18:21]
	v_or_b32_e32 v34, 6, v50
	v_mfma_f32_16x16x32_bf16 v[6:9], v[26:29], v[42:45], v[6:9]
	v_lshl_or_b32 v26, v34, 10, v198
	ds_read_b128 v[26:29], v26
	v_lshl_or_b32 v34, v34, 8, v204
	ds_read_b128 v[34:37], v34
	ds_read_b128 v[42:45], v216
	s_waitcnt lgkmcnt(0)
	v_mfma_f32_16x16x32_bf16 v[18:21], v[34:37], v[42:45], v[18:21]
	v_or_b32_e32 v34, 7, v50
	v_mfma_f32_16x16x32_bf16 v[6:9], v[26:29], v[42:45], v[6:9]
	v_lshl_or_b32 v26, v34, 10, v198
	ds_read_b128 v[26:29], v26
	v_lshl_or_b32 v34, v34, 8, v204
	ds_read_b128 v[34:37], v34
	ds_read_b128 v[42:45], v213
	s_waitcnt lgkmcnt(0)
	v_mfma_f32_16x16x32_bf16 v[162:165], v[26:29], v[42:45], v[6:9]
	s_waitcnt vmcnt(31)
	s_nop 1
	v_cvt_pk_bf16_f32 v6, v102, v103
	v_cvt_pk_bf16_f32 v7, v104, v105
	ds_write_b64 v212, v[6:7]
	s_waitcnt vmcnt(30)
	v_cvt_pk_bf16_f32 v6, v98, v99
	v_cvt_pk_bf16_f32 v7, v100, v101
	ds_write_b64 v211, v[6:7] offset:512
	s_waitcnt vmcnt(29)
	v_cvt_pk_bf16_f32 v6, v110, v111
	v_cvt_pk_bf16_f32 v7, v112, v113
	ds_write_b64 v210, v[6:7] offset:1024
	s_waitcnt vmcnt(28)
	v_cvt_pk_bf16_f32 v6, v106, v107
	v_cvt_pk_bf16_f32 v7, v108, v109
	ds_write_b64 v209, v[6:7] offset:1536
	s_waitcnt vmcnt(27)
	v_cvt_pk_bf16_f32 v6, v118, v119
	v_cvt_pk_bf16_f32 v7, v120, v121
	ds_write_b64 v208, v[6:7] offset:2048
	s_waitcnt vmcnt(26)
	v_cvt_pk_bf16_f32 v6, v114, v115
	v_cvt_pk_bf16_f32 v7, v116, v117
	ds_write_b64 v207, v[6:7] offset:2560
	s_waitcnt vmcnt(25)
	v_cvt_pk_bf16_f32 v6, v126, v127
	v_cvt_pk_bf16_f32 v7, v128, v129
	ds_write_b64 v206, v[6:7] offset:3072
	s_waitcnt vmcnt(24)
	v_cvt_pk_bf16_f32 v6, v122, v123
	v_cvt_pk_bf16_f32 v7, v124, v125
	ds_write_b64 v205, v[6:7] offset:3584
	s_waitcnt vmcnt(23)
	v_cvt_pk_bf16_f32 v6, v134, v135
	v_cvt_pk_bf16_f32 v7, v136, v137
	ds_write_b64 v231, v[6:7] offset:4096
	s_waitcnt vmcnt(22)
	v_cvt_pk_bf16_f32 v6, v130, v131
	v_cvt_pk_bf16_f32 v7, v132, v133
	ds_write_b64 v230, v[6:7] offset:4608
	s_waitcnt vmcnt(21)
	v_cvt_pk_bf16_f32 v6, v142, v143
	v_cvt_pk_bf16_f32 v7, v144, v145
	ds_write_b64 v229, v[6:7] offset:5120
	s_waitcnt vmcnt(20)
	v_cvt_pk_bf16_f32 v6, v138, v139
	v_cvt_pk_bf16_f32 v7, v140, v141
	ds_write_b64 v228, v[6:7] offset:5632
	s_waitcnt vmcnt(19)
	v_cvt_pk_bf16_f32 v6, v170, v171
	v_cvt_pk_bf16_f32 v7, v172, v173
	ds_write_b64 v227, v[6:7] offset:6144
	s_waitcnt vmcnt(18)
	v_cvt_pk_bf16_f32 v6, v158, v159
	v_mov_b32_e32 v106, 0x1000
	v_cvt_pk_bf16_f32 v7, v160, v161
	ds_write_b64 v226, v[6:7] offset:6656
	s_waitcnt vmcnt(17)
	v_cvt_pk_bf16_f32 v6, v190, v191
	v_bitop3_b32 v107, v233, s19, v106 bitop3:0xde
	v_mfma_f32_16x16x32_bf16 v[166:169], v[34:37], v[42:45], v[18:21]
	v_cvt_pk_bf16_f32 v7, v192, v193
	ds_write_b64 v225, v[6:7] offset:7168
	s_waitcnt vmcnt(16)
	v_cvt_pk_bf16_f32 v6, v186, v187
	v_bitop3_b32 v26, v233, s17, v106 bitop3:0xde
	v_bitop3_b32 v34, v233, s11, v106 bitop3:0xde
	v_bitop3_b32 v18, v233, s16, v106 bitop3:0xde
	v_bitop3_b32 v42, v233, s13, v106 bitop3:0xde
	v_bitop3_b32 v50, v233, s10, v106 bitop3:0xde
	v_bitop3_b32 v58, v233, s12, v106 bitop3:0xde
	v_bitop3_b32 v66, v233, s1, v106 bitop3:0xde
	v_bitop3_b32 v74, v233, s18, v106 bitop3:0xde
	v_bitop3_b32 v82, v233, s23, v106 bitop3:0xde
	v_bitop3_b32 v90, v233, s22, v106 bitop3:0xde
	v_bitop3_b32 v98, v233, s21, v106 bitop3:0xde
	v_bitop3_b32 v102, v233, s20, v106 bitop3:0xde
	buffer_load_dwordx4 v[110:113], v107, s[4:7], 0 offen nt
	v_bitop3_b32 v107, v233, s15, v106 bitop3:0xde
	v_bitop3_b32 v106, v233, s14, v106 bitop3:0xde
	v_cvt_pk_bf16_f32 v7, v188, v189
	ds_write_b64 v224, v[6:7] offset:7680
	v_bitop3_b32 v6, v203, s24, v196 bitop3:0x36
	buffer_load_dwordx4 v[42:45], v42, s[4:7], 0 offen nt
	s_nop 0
	buffer_load_dwordx4 v[50:53], v50, s[4:7], 0 offen nt
	s_nop 0
	buffer_load_dwordx4 v[58:61], v58, s[4:7], 0 offen nt
	s_nop 0
	buffer_load_dwordx4 v[66:69], v66, s[4:7], 0 offen nt
	s_nop 0
	buffer_load_dwordx4 v[74:77], v74, s[4:7], 0 offen nt
	s_nop 0
	buffer_load_dwordx4 v[82:85], v82, s[4:7], 0 offen nt
	s_nop 0
	buffer_load_dwordx4 v[90:93], v90, s[4:7], 0 offen nt
	s_nop 0
	buffer_load_dwordx4 v[98:101], v98, s[4:7], 0 offen nt
	s_nop 0
	buffer_load_dwordx4 v[102:105], v102, s[4:7], 0 offen nt
	s_nop 0
	buffer_load_dwordx4 v[126:129], v106, s[4:7], 0 offen nt
	buffer_load_dwordx4 v[118:121], v107, s[4:7], 0 offen nt
	s_nop 0
	buffer_load_dwordx4 v[6:9], v6, s[4:7], 0 offen nt
	s_nop 0
	buffer_load_dwordx4 v[18:21], v18, s[4:7], 0 offen nt
	s_nop 0
	buffer_load_dwordx4 v[26:29], v26, s[4:7], 0 offen nt
	s_nop 0
	buffer_load_dwordx4 v[34:37], v34, s[4:7], 0 offen nt
	v_add_u32_e32 v106, 16, v232
	v_and_b32_e32 v138, 56, v106
	v_lshl_or_b32 v106, v138, 10, v198
	ds_read_b128 v[106:109], v106
	v_lshl_or_b32 v114, v138, 8, v204
	ds_read_b128 v[114:117], v114
	ds_read_b128 v[122:125], v223
	v_or_b32_e32 v130, 1, v138
	s_waitcnt vmcnt(31)
	v_cvt_pk_bf16_f32 v2, v2, v3
	s_waitcnt lgkmcnt(0)
	v_mfma_f32_16x16x32_bf16 v[114:117], v[114:117], v[122:125], v[166:169]
	v_cvt_pk_bf16_f32 v3, v4, v5
	v_mfma_f32_16x16x32_bf16 v[106:109], v[106:109], v[122:125], v[162:165]
	v_lshl_or_b32 v122, v130, 10, v198
	ds_read_b128 v[122:125], v122
	v_lshl_or_b32 v130, v130, 8, v204
	ds_read_b128 v[130:133], v130
	ds_read_b128 v[134:137], v222
	s_waitcnt lgkmcnt(0)
	v_mfma_f32_16x16x32_bf16 v[114:117], v[130:133], v[134:137], v[114:117]
	v_or_b32_e32 v130, 2, v138
	v_mfma_f32_16x16x32_bf16 v[106:109], v[122:125], v[134:137], v[106:109]
	v_lshl_or_b32 v122, v130, 10, v198
	ds_read_b128 v[122:125], v122
	v_lshl_or_b32 v130, v130, 8, v204
	ds_read_b128 v[130:133], v130
	ds_read_b128 v[134:137], v221
	s_waitcnt lgkmcnt(0)
	v_mfma_f32_16x16x32_bf16 v[114:117], v[130:133], v[134:137], v[114:117]
	v_or_b32_e32 v130, 3, v138
	v_mfma_f32_16x16x32_bf16 v[106:109], v[122:125], v[134:137], v[106:109]
	v_lshl_or_b32 v122, v130, 10, v198
	ds_read_b128 v[122:125], v122
	v_lshl_or_b32 v130, v130, 8, v204
	ds_read_b128 v[130:133], v130
	ds_read_b128 v[134:137], v219
	s_waitcnt lgkmcnt(0)
	v_mfma_f32_16x16x32_bf16 v[114:117], v[130:133], v[134:137], v[114:117]
	v_or_b32_e32 v130, 4, v138
	v_mfma_f32_16x16x32_bf16 v[106:109], v[122:125], v[134:137], v[106:109]
	v_lshl_or_b32 v122, v130, 10, v198
	ds_read_b128 v[122:125], v122
	v_lshl_or_b32 v130, v130, 8, v204
	ds_read_b128 v[130:133], v130
	ds_read_b128 v[134:137], v218
	s_waitcnt lgkmcnt(0)
	v_mfma_f32_16x16x32_bf16 v[114:117], v[130:133], v[134:137], v[114:117]
	v_or_b32_e32 v130, 5, v138
	v_mfma_f32_16x16x32_bf16 v[106:109], v[122:125], v[134:137], v[106:109]
	v_lshl_or_b32 v122, v130, 10, v198
	ds_read_b128 v[122:125], v122
	v_lshl_or_b32 v130, v130, 8, v204
	ds_read_b128 v[130:133], v130
	ds_read_b128 v[134:137], v217
	s_waitcnt lgkmcnt(0)
	v_mfma_f32_16x16x32_bf16 v[114:117], v[130:133], v[134:137], v[114:117]
	v_or_b32_e32 v130, 6, v138
	v_mfma_f32_16x16x32_bf16 v[106:109], v[122:125], v[134:137], v[106:109]
	v_lshl_or_b32 v122, v130, 10, v198
	ds_read_b128 v[122:125], v122
	v_lshl_or_b32 v130, v130, 8, v204
	ds_read_b128 v[130:133], v130
	ds_read_b128 v[134:137], v216
	s_waitcnt lgkmcnt(0)
	v_mfma_f32_16x16x32_bf16 v[114:117], v[130:133], v[134:137], v[114:117]
	v_or_b32_e32 v130, 7, v138
	v_mfma_f32_16x16x32_bf16 v[106:109], v[122:125], v[134:137], v[106:109]
	v_lshl_or_b32 v122, v130, 10, v198
	v_lshl_or_b32 v130, v130, 8, v204
	ds_read_b128 v[122:125], v122
	ds_read_b128 v[134:137], v130
	ds_read_b128 v[138:141], v213
	ds_write_b64 v212, v[2:3]
	s_waitcnt vmcnt(30)
	v_cvt_pk_bf16_f32 v2, v10, v11
	v_cvt_pk_bf16_f32 v3, v12, v13
	ds_write_b64 v211, v[2:3] offset:512
	s_waitcnt vmcnt(29)
	v_cvt_pk_bf16_f32 v2, v14, v15
	v_cvt_pk_bf16_f32 v3, v16, v17
	ds_write_b64 v210, v[2:3] offset:1024
	s_waitcnt vmcnt(28)
	v_cvt_pk_bf16_f32 v2, v22, v23
	v_cvt_pk_bf16_f32 v3, v24, v25
	ds_write_b64 v209, v[2:3] offset:1536
	s_waitcnt vmcnt(27)
	v_cvt_pk_bf16_f32 v2, v30, v31
	v_cvt_pk_bf16_f32 v3, v32, v33
	ds_write_b64 v208, v[2:3] offset:2048
	s_waitcnt vmcnt(26)
	v_cvt_pk_bf16_f32 v2, v38, v39
	v_cvt_pk_bf16_f32 v3, v40, v41
	ds_write_b64 v207, v[2:3] offset:2560
	s_waitcnt vmcnt(25)
	v_cvt_pk_bf16_f32 v2, v46, v47
	v_cvt_pk_bf16_f32 v3, v48, v49
	ds_write_b64 v206, v[2:3] offset:3072
	s_waitcnt vmcnt(24)
	v_cvt_pk_bf16_f32 v2, v54, v55
	v_cvt_pk_bf16_f32 v3, v56, v57
	ds_write_b64 v205, v[2:3] offset:3584
	s_waitcnt vmcnt(23)
	v_cvt_pk_bf16_f32 v2, v62, v63
	v_cvt_pk_bf16_f32 v3, v64, v65
	ds_write_b64 v231, v[2:3] offset:4096
	s_waitcnt vmcnt(22)
	v_cvt_pk_bf16_f32 v2, v70, v71
	v_cvt_pk_bf16_f32 v3, v72, v73
	ds_write_b64 v230, v[2:3] offset:4608
	s_waitcnt vmcnt(21)
	v_cvt_pk_bf16_f32 v2, v78, v79
	v_cvt_pk_bf16_f32 v3, v80, v81
	ds_write_b64 v229, v[2:3] offset:5120
	s_waitcnt vmcnt(20)
	v_cvt_pk_bf16_f32 v2, v86, v87
	v_cvt_pk_bf16_f32 v3, v88, v89
	ds_write_b64 v228, v[2:3] offset:5632
	s_waitcnt vmcnt(19)
	v_cvt_pk_bf16_f32 v2, v94, v95
	v_cvt_pk_bf16_f32 v3, v96, v97
	ds_write_b64 v227, v[2:3] offset:6144
	s_waitcnt vmcnt(18)
	v_cvt_pk_bf16_f32 v2, v146, v147
	v_cvt_pk_bf16_f32 v3, v148, v149
	ds_write_b64 v226, v[2:3] offset:6656
	s_waitcnt vmcnt(17)
	v_cvt_pk_bf16_f32 v2, v150, v151
	v_cvt_pk_bf16_f32 v3, v152, v153
	ds_write_b64 v225, v[2:3] offset:7168
	s_waitcnt vmcnt(16)
	v_cvt_pk_bf16_f32 v2, v154, v155
	v_cvt_pk_bf16_f32 v3, v156, v157
	ds_write_b64 v224, v[2:3] offset:7680
	v_lshlrev_b32_e32 v2, 10, v234
	s_waitcnt lgkmcnt(14)
	v_mfma_f32_16x16x32_bf16 v[130:133], v[122:125], v[138:141], v[106:109]
	v_and_or_b32 v122, v2, s0, v203
	buffer_load_dwordx4 v[2:5], v122, s[4:7], 0 offen nt
	v_or_b32_e32 v10, 0x2000, v122
	v_mfma_f32_16x16x32_bf16 v[134:137], v[134:137], v[138:141], v[114:117]
	v_or_b32_e32 v14, 0x4000, v122
	v_or_b32_e32 v22, 0x6000, v122
	v_or_b32_e32 v30, 0x8000, v122
	v_or_b32_e32 v38, 0xa000, v122
	v_or_b32_e32 v46, 0xc000, v122
	v_or_b32_e32 v54, 0xe000, v122
	v_or_b32_e32 v62, 0x10000, v122
	v_or_b32_e32 v70, 0x12000, v122
	v_or_b32_e32 v78, 0x14000, v122
	v_or_b32_e32 v86, 0x16000, v122
	v_or_b32_e32 v94, 0x18000, v122
	v_or_b32_e32 v106, 0x1a000, v122
	v_or_b32_e32 v114, 0x1c000, v122
	v_or_b32_e32 v122, 0x1e000, v122
	buffer_load_dwordx4 v[54:57], v54, s[4:7], 0 offen nt
	s_nop 0
	buffer_load_dwordx4 v[62:65], v62, s[4:7], 0 offen nt
	s_nop 0
	buffer_load_dwordx4 v[70:73], v70, s[4:7], 0 offen nt
	s_nop 0
	buffer_load_dwordx4 v[78:81], v78, s[4:7], 0 offen nt
	s_nop 0
	buffer_load_dwordx4 v[86:89], v86, s[4:7], 0 offen nt
	s_nop 0
	buffer_load_dwordx4 v[94:97], v94, s[4:7], 0 offen nt
	s_nop 0
	buffer_load_dwordx4 v[106:109], v106, s[4:7], 0 offen nt
	s_nop 0
	buffer_load_dwordx4 v[114:117], v114, s[4:7], 0 offen nt
	s_nop 0
	buffer_load_dwordx4 v[122:125], v122, s[4:7], 0 offen nt
	s_nop 0
	buffer_load_dwordx4 v[10:13], v10, s[4:7], 0 offen nt
	s_nop 0
	buffer_load_dwordx4 v[14:17], v14, s[4:7], 0 offen nt
	s_nop 0
	buffer_load_dwordx4 v[22:25], v22, s[4:7], 0 offen nt
	s_nop 0
	buffer_load_dwordx4 v[30:33], v30, s[4:7], 0 offen nt
	s_nop 0
	buffer_load_dwordx4 v[38:41], v38, s[4:7], 0 offen nt
	s_nop 0
	buffer_load_dwordx4 v[46:49], v46, s[4:7], 0 offen nt
	v_lshlrev_b32_e32 v138, 3, v235
	v_and_b32_e32 v150, 56, v138
	v_lshl_or_b32 v138, v150, 10, v198
	ds_read_b128 v[138:141], v138
	v_lshl_or_b32 v142, v150, 8, v204
	ds_read_b128 v[142:145], v142
	ds_read_b128 v[146:149], v223
	s_waitcnt vmcnt(19)
	v_cvt_pk_bf16_f32 v6, v6, v7
	v_cvt_pk_bf16_f32 v7, v8, v9
	s_waitcnt lgkmcnt(0)
	v_mfma_f32_16x16x32_bf16 v[134:137], v[142:145], v[146:149], v[134:137]
	v_or_b32_e32 v142, 1, v150
	v_mfma_f32_16x16x32_bf16 v[130:133], v[138:141], v[146:149], v[130:133]
	v_lshl_or_b32 v138, v142, 10, v198
	ds_read_b128 v[138:141], v138
	v_lshl_or_b32 v142, v142, 8, v204
	ds_read_b128 v[142:145], v142
	ds_read_b128 v[146:149], v222
	s_waitcnt lgkmcnt(0)
	v_mfma_f32_16x16x32_bf16 v[134:137], v[142:145], v[146:149], v[134:137]
	v_or_b32_e32 v142, 2, v150
	v_mfma_f32_16x16x32_bf16 v[130:133], v[138:141], v[146:149], v[130:133]
	v_lshl_or_b32 v138, v142, 10, v198
	ds_read_b128 v[138:141], v138
	v_lshl_or_b32 v142, v142, 8, v204
	ds_read_b128 v[142:145], v142
	ds_read_b128 v[146:149], v221
	s_waitcnt lgkmcnt(0)
	v_mfma_f32_16x16x32_bf16 v[134:137], v[142:145], v[146:149], v[134:137]
	v_or_b32_e32 v142, 3, v150
	v_mfma_f32_16x16x32_bf16 v[130:133], v[138:141], v[146:149], v[130:133]
	v_lshl_or_b32 v138, v142, 10, v198
	ds_read_b128 v[138:141], v138
	v_lshl_or_b32 v142, v142, 8, v204
	ds_read_b128 v[142:145], v142
	ds_read_b128 v[146:149], v219
	s_waitcnt lgkmcnt(0)
	v_mfma_f32_16x16x32_bf16 v[134:137], v[142:145], v[146:149], v[134:137]
	v_or_b32_e32 v142, 4, v150
	v_mfma_f32_16x16x32_bf16 v[130:133], v[138:141], v[146:149], v[130:133]
	v_lshl_or_b32 v138, v142, 10, v198
	ds_read_b128 v[138:141], v138
	v_lshl_or_b32 v142, v142, 8, v204
	ds_read_b128 v[142:145], v142
	ds_read_b128 v[146:149], v218
	s_waitcnt lgkmcnt(0)
	v_mfma_f32_16x16x32_bf16 v[134:137], v[142:145], v[146:149], v[134:137]
	v_or_b32_e32 v142, 5, v150
	v_mfma_f32_16x16x32_bf16 v[130:133], v[138:141], v[146:149], v[130:133]
	v_lshl_or_b32 v138, v142, 10, v198
	ds_read_b128 v[138:141], v138
	v_lshl_or_b32 v142, v142, 8, v204
	ds_read_b128 v[142:145], v142
	ds_read_b128 v[146:149], v217
	s_waitcnt lgkmcnt(0)
	v_mfma_f32_16x16x32_bf16 v[134:137], v[142:145], v[146:149], v[134:137]
	v_or_b32_e32 v142, 6, v150
	v_mfma_f32_16x16x32_bf16 v[130:133], v[138:141], v[146:149], v[130:133]
	v_lshl_or_b32 v138, v142, 10, v198
	ds_read_b128 v[138:141], v138
	v_lshl_or_b32 v142, v142, 8, v204
	ds_read_b128 v[142:145], v142
	ds_read_b128 v[146:149], v216
	s_waitcnt lgkmcnt(0)
	v_mfma_f32_16x16x32_bf16 v[134:137], v[142:145], v[146:149], v[134:137]
	v_or_b32_e32 v142, 7, v150
	v_mfma_f32_16x16x32_bf16 v[130:133], v[138:141], v[146:149], v[130:133]
	v_lshl_or_b32 v138, v142, 10, v198
	v_lshl_or_b32 v142, v142, 8, v204
	ds_read_b128 v[138:141], v138
	ds_read_b128 v[142:145], v142
	ds_read_b128 v[146:149], v213
	ds_write_b64 v212, v[6:7]
	s_waitcnt vmcnt(18)
	v_cvt_pk_bf16_f32 v6, v18, v19
	v_cvt_pk_bf16_f32 v7, v20, v21
	ds_write_b64 v211, v[6:7] offset:512
	s_waitcnt vmcnt(17)
	v_cvt_pk_bf16_f32 v6, v26, v27
	v_cvt_pk_bf16_f32 v7, v28, v29
	ds_write_b64 v210, v[6:7] offset:1024
	s_waitcnt vmcnt(16)
	v_cvt_pk_bf16_f32 v6, v34, v35
	v_cvt_pk_bf16_f32 v7, v36, v37
	ds_write_b64 v209, v[6:7] offset:1536
	v_cvt_pk_bf16_f32 v6, v42, v43
	v_cvt_pk_bf16_f32 v7, v44, v45
	ds_write_b64 v208, v[6:7] offset:2048
	v_cvt_pk_bf16_f32 v6, v50, v51
	v_cvt_pk_bf16_f32 v7, v52, v53
	ds_write_b64 v207, v[6:7] offset:2560
	v_cvt_pk_bf16_f32 v6, v58, v59
	v_cvt_pk_bf16_f32 v7, v60, v61
	ds_write_b64 v206, v[6:7] offset:3072
	v_cvt_pk_bf16_f32 v6, v66, v67
	v_cvt_pk_bf16_f32 v7, v68, v69
	ds_write_b64 v205, v[6:7] offset:3584
	v_cvt_pk_bf16_f32 v6, v74, v75
	v_cvt_pk_bf16_f32 v7, v76, v77
	ds_write_b64 v231, v[6:7] offset:4096
	v_cvt_pk_bf16_f32 v6, v82, v83
	v_cvt_pk_bf16_f32 v7, v84, v85
	ds_write_b64 v230, v[6:7] offset:4608
	v_cvt_pk_bf16_f32 v6, v90, v91
	v_cvt_pk_bf16_f32 v7, v92, v93
	ds_write_b64 v229, v[6:7] offset:5120
	v_cvt_pk_bf16_f32 v6, v98, v99
	v_cvt_pk_bf16_f32 v7, v100, v101
	ds_write_b64 v228, v[6:7] offset:5632
	v_cvt_pk_bf16_f32 v6, v102, v103
	v_cvt_pk_bf16_f32 v7, v104, v105
	ds_write_b64 v227, v[6:7] offset:6144
	v_cvt_pk_bf16_f32 v6, v110, v111
	v_cvt_pk_bf16_f32 v7, v112, v113
	ds_write_b64 v226, v[6:7] offset:6656
	v_cvt_pk_bf16_f32 v6, v118, v119
	v_cvt_pk_bf16_f32 v7, v120, v121
	ds_write_b64 v225, v[6:7] offset:7168
	v_cvt_pk_bf16_f32 v6, v126, v127
	v_cvt_pk_bf16_f32 v7, v128, v129
	ds_write_b64 v224, v[6:7] offset:7680
	v_add_u32_e32 v6, 0x1800, v196
	v_and_or_b32 v126, v6, s0, v203
	buffer_load_dwordx4 v[6:9], v126, s[4:7], 0 offen nt
	v_or_b32_e32 v18, 0x2000, v126
	v_or_b32_e32 v26, 0x4000, v126
	v_or_b32_e32 v34, 0x6000, v126
	v_or_b32_e32 v42, 0x8000, v126
	v_or_b32_e32 v50, 0xa000, v126
	v_or_b32_e32 v58, 0xc000, v126
	v_or_b32_e32 v66, 0xe000, v126
	v_or_b32_e32 v74, 0x10000, v126
	v_or_b32_e32 v82, 0x12000, v126
	v_or_b32_e32 v90, 0x14000, v126
	v_or_b32_e32 v98, 0x16000, v126
	v_or_b32_e32 v102, 0x18000, v126
	v_or_b32_e32 v110, 0x1a000, v126
	v_or_b32_e32 v118, 0x1c000, v126
	v_or_b32_e32 v126, 0x1e000, v126
	buffer_load_dwordx4 v[50:53], v50, s[4:7], 0 offen nt
	s_waitcnt lgkmcnt(14)
	v_mfma_f32_16x16x32_bf16 v[130:133], v[138:141], v[146:149], v[130:133]
	buffer_load_dwordx4 v[58:61], v58, s[4:7], 0 offen nt
	s_nop 0
	buffer_load_dwordx4 v[66:69], v66, s[4:7], 0 offen nt
	v_mfma_f32_16x16x32_bf16 v[134:137], v[142:145], v[146:149], v[134:137]
	buffer_load_dwordx4 v[74:77], v74, s[4:7], 0 offen nt
	v_add_u32_e32 v142, 7, v200
	buffer_load_dwordx4 v[82:85], v82, s[4:7], 0 offen nt
	s_nop 0
	buffer_load_dwordx4 v[90:93], v90, s[4:7], 0 offen nt
	s_nop 0
	buffer_load_dwordx4 v[98:101], v98, s[4:7], 0 offen nt
	s_nop 0
	buffer_load_dwordx4 v[102:105], v102, s[4:7], 0 offen nt
	s_nop 0
	buffer_load_dwordx4 v[110:113], v110, s[4:7], 0 offen nt
	s_nop 0
	buffer_load_dwordx4 v[118:121], v118, s[4:7], 0 offen nt
	s_nop 0
	buffer_load_dwordx4 v[126:129], v126, s[4:7], 0 offen nt
	s_nop 0
	buffer_load_dwordx4 v[18:21], v18, s[4:7], 0 offen nt
	s_nop 0
	buffer_load_dwordx4 v[26:29], v26, s[4:7], 0 offen nt
	s_nop 0
	buffer_load_dwordx4 v[34:37], v34, s[4:7], 0 offen nt
	s_nop 0
	buffer_load_dwordx4 v[42:45], v42, s[4:7], 0 offen nt
	v_xor_b32_e32 v143, 32, v232
	v_lshl_or_b32 v138, v143, 10, v198
	ds_read_b128 v[138:141], v138
	v_lshl_or_b32 v143, v143, 8, v204
	ds_read_b128 v[144:147], v143
	ds_read_b128 v[148:151], v223
	v_bitop3_b32 v143, v232, 1, 32 bitop3:0xde
	s_waitcnt vmcnt(31)
	v_cvt_pk_bf16_f32 v2, v2, v3
	s_waitcnt lgkmcnt(0)
	v_mfma_f32_16x16x32_bf16 v[134:137], v[144:147], v[148:151], v[134:137]
	v_cvt_pk_bf16_f32 v3, v4, v5
	v_mfma_f32_16x16x32_bf16 v[130:133], v[138:141], v[148:151], v[130:133]
	v_lshl_or_b32 v138, v143, 10, v198
	ds_read_b128 v[138:141], v138
	v_lshl_or_b32 v143, v143, 8, v204
	ds_read_b128 v[144:147], v143
	ds_read_b128 v[148:151], v222
	v_bitop3_b32 v143, v232, 2, 32 bitop3:0xde
	s_waitcnt lgkmcnt(0)
	v_mfma_f32_16x16x32_bf16 v[134:137], v[144:147], v[148:151], v[134:137]
	v_mfma_f32_16x16x32_bf16 v[130:133], v[138:141], v[148:151], v[130:133]
	v_lshl_or_b32 v138, v143, 10, v198
	ds_read_b128 v[138:141], v138
	v_lshl_or_b32 v143, v143, 8, v204
	ds_read_b128 v[144:147], v143
	ds_read_b128 v[148:151], v221
	v_bitop3_b32 v143, v232, 3, 32 bitop3:0xde
	s_waitcnt lgkmcnt(0)
	v_mfma_f32_16x16x32_bf16 v[130:133], v[138:141], v[148:151], v[130:133]
	v_lshl_or_b32 v138, v143, 10, v198
	ds_read_b128 v[138:141], v138
	v_lshl_or_b32 v143, v143, 8, v204
	v_mfma_f32_16x16x32_bf16 v[134:137], v[144:147], v[148:151], v[134:137]
	ds_read_b128 v[144:147], v143
	ds_read_b128 v[148:151], v219
	v_bitop3_b32 v143, v232, 4, 32 bitop3:0xde
	s_waitcnt lgkmcnt(0)
	v_mfma_f32_16x16x32_bf16 v[130:133], v[138:141], v[148:151], v[130:133]
	v_lshl_or_b32 v138, v143, 10, v198
	ds_read_b128 v[138:141], v138
	v_lshl_or_b32 v143, v143, 8, v204
	v_mfma_f32_16x16x32_bf16 v[134:137], v[144:147], v[148:151], v[134:137]
	ds_read_b128 v[144:147], v143
	ds_read_b128 v[148:151], v218
	v_bitop3_b32 v143, v232, 5, 32 bitop3:0xde
	s_waitcnt lgkmcnt(0)
	v_mfma_f32_16x16x32_bf16 v[130:133], v[138:141], v[148:151], v[130:133]
	v_lshl_or_b32 v138, v143, 10, v198
	ds_read_b128 v[138:141], v138
	v_lshl_or_b32 v143, v143, 8, v204
	v_mfma_f32_16x16x32_bf16 v[134:137], v[144:147], v[148:151], v[134:137]
	ds_read_b128 v[144:147], v143
	ds_read_b128 v[148:151], v217
	v_bitop3_b32 v143, v232, 6, 32 bitop3:0xde
	s_waitcnt lgkmcnt(0)
	v_mfma_f32_16x16x32_bf16 v[130:133], v[138:141], v[148:151], v[130:133]
	v_lshl_or_b32 v138, v143, 10, v198
	ds_read_b128 v[138:141], v138
	v_lshl_or_b32 v143, v143, 8, v204
	v_mfma_f32_16x16x32_bf16 v[134:137], v[144:147], v[148:151], v[134:137]
	ds_read_b128 v[144:147], v143
	ds_read_b128 v[148:151], v216
	v_bitop3_b32 v143, v232, 7, 32 bitop3:0xde
	s_waitcnt lgkmcnt(0)
	v_mfma_f32_16x16x32_bf16 v[130:133], v[138:141], v[148:151], v[130:133]
	v_lshl_or_b32 v138, v143, 10, v198
	v_lshl_or_b32 v143, v143, 8, v204
	ds_read_b128 v[138:141], v138
	v_mfma_f32_16x16x32_bf16 v[134:137], v[144:147], v[148:151], v[134:137]
	ds_read_b128 v[144:147], v143
	ds_read_b128 v[148:151], v213
	ds_write_b64 v212, v[2:3]
	s_waitcnt vmcnt(21)
	v_cvt_pk_bf16_f32 v2, v10, v11
	v_cvt_pk_bf16_f32 v3, v12, v13
	ds_write_b64 v211, v[2:3] offset:512
	s_waitcnt vmcnt(20)
	v_cvt_pk_bf16_f32 v2, v14, v15
	v_cvt_pk_bf16_f32 v3, v16, v17
	ds_write_b64 v210, v[2:3] offset:1024
	s_waitcnt vmcnt(19)
	v_cvt_pk_bf16_f32 v2, v22, v23
	v_cvt_pk_bf16_f32 v3, v24, v25
	ds_write_b64 v209, v[2:3] offset:1536
	s_waitcnt vmcnt(18)
	v_cvt_pk_bf16_f32 v2, v30, v31
	v_cvt_pk_bf16_f32 v3, v32, v33
	ds_write_b64 v208, v[2:3] offset:2048
	s_waitcnt vmcnt(17)
	v_cvt_pk_bf16_f32 v2, v38, v39
	v_cvt_pk_bf16_f32 v3, v40, v41
	ds_write_b64 v207, v[2:3] offset:2560
	s_waitcnt vmcnt(16)
	v_cvt_pk_bf16_f32 v2, v46, v47
	v_cvt_pk_bf16_f32 v3, v48, v49
	ds_write_b64 v206, v[2:3] offset:3072
	v_cvt_pk_bf16_f32 v2, v54, v55
	v_cvt_pk_bf16_f32 v3, v56, v57
	ds_write_b64 v205, v[2:3] offset:3584
	v_cvt_pk_bf16_f32 v2, v62, v63
	v_cvt_pk_bf16_f32 v3, v64, v65
	ds_write_b64 v231, v[2:3] offset:4096
	v_cvt_pk_bf16_f32 v2, v70, v71
	v_cvt_pk_bf16_f32 v3, v72, v73
	ds_write_b64 v230, v[2:3] offset:4608
	v_cvt_pk_bf16_f32 v2, v78, v79
	v_cvt_pk_bf16_f32 v3, v80, v81
	ds_write_b64 v229, v[2:3] offset:5120
	v_cvt_pk_bf16_f32 v2, v86, v87
	v_cvt_pk_bf16_f32 v3, v88, v89
	ds_write_b64 v228, v[2:3] offset:5632
	v_cvt_pk_bf16_f32 v2, v94, v95
	v_cvt_pk_bf16_f32 v3, v96, v97
	ds_write_b64 v227, v[2:3] offset:6144
	v_cvt_pk_bf16_f32 v2, v106, v107
	v_cvt_pk_bf16_f32 v3, v108, v109
	ds_write_b64 v226, v[2:3] offset:6656
	v_cvt_pk_bf16_f32 v2, v114, v115
	v_cvt_pk_bf16_f32 v3, v116, v117
	ds_write_b64 v225, v[2:3] offset:7168
	v_cvt_pk_bf16_f32 v2, v122, v123
	v_cvt_pk_bf16_f32 v3, v124, v125
	ds_write_b64 v224, v[2:3] offset:7680
	v_lshlrev_b32_e32 v2, 10, v142
	v_and_or_b32 v2, v2, s0, v203
	v_or_b32_e32 v3, 0x2000, v2
	buffer_load_dwordx4 v[10:13], v2, s[4:7], 0 offen nt
	buffer_load_dwordx4 v[14:17], v3, s[4:7], 0 offen nt
	v_or_b32_e32 v3, 0x4000, v2
	buffer_load_dwordx4 v[22:25], v3, s[4:7], 0 offen nt
	v_or_b32_e32 v3, 0x6000, v2
	buffer_load_dwordx4 v[30:33], v3, s[4:7], 0 offen nt
	v_or_b32_e32 v3, 0x8000, v2
	buffer_load_dwordx4 v[38:41], v3, s[4:7], 0 offen nt
	v_or_b32_e32 v3, 0xa000, v2
	buffer_load_dwordx4 v[46:49], v3, s[4:7], 0 offen nt
	v_or_b32_e32 v3, 0xc000, v2
	buffer_load_dwordx4 v[54:57], v3, s[4:7], 0 offen nt
	v_or_b32_e32 v3, 0xe000, v2
	buffer_load_dwordx4 v[62:65], v3, s[4:7], 0 offen nt
	v_or_b32_e32 v3, 0x10000, v2
	buffer_load_dwordx4 v[70:73], v3, s[4:7], 0 offen nt
	v_or_b32_e32 v3, 0x12000, v2
	buffer_load_dwordx4 v[78:81], v3, s[4:7], 0 offen nt
	v_or_b32_e32 v3, 0x14000, v2
	buffer_load_dwordx4 v[86:89], v3, s[4:7], 0 offen nt
	v_or_b32_e32 v3, 0x16000, v2
	buffer_load_dwordx4 v[94:97], v3, s[4:7], 0 offen nt
	v_or_b32_e32 v3, 0x18000, v2
	buffer_load_dwordx4 v[106:109], v3, s[4:7], 0 offen nt
	v_or_b32_e32 v3, 0x1a000, v2
	buffer_load_dwordx4 v[114:117], v3, s[4:7], 0 offen nt
	v_or_b32_e32 v3, 0x1c000, v2
	v_or_b32_e32 v2, 0x1e000, v2
	s_waitcnt lgkmcnt(14)
	v_mfma_f32_16x16x32_bf16 v[138:141], v[138:141], v[148:151], v[130:133]
	buffer_load_dwordx4 v[122:125], v3, s[4:7], 0 offen nt
	s_nop 1
	buffer_load_dwordx4 v[130:133], v2, s[4:7], 0 offen nt
	v_mfma_f32_16x16x32_bf16 v[134:137], v[144:147], v[148:151], v[134:137]
	v_lshlrev_b32_e32 v2, 3, v234
	v_and_b32_e32 v143, 56, v2
	v_lshl_or_b32 v2, v143, 10, v198
	v_lshl_or_b32 v152, v143, 8, v204
	ds_read_b128 v[2:5], v2
	ds_read_b128 v[144:147], v223
	ds_read_b128 v[148:151], v222
	ds_read_b128 v[152:155], v152
	v_or_b32_e32 v156, 1, v143
	v_lshl_or_b32 v157, v156, 10, v198
	s_waitcnt lgkmcnt(2)
	v_mfma_f32_16x16x32_bf16 v[2:5], v[2:5], v[144:147], v[138:141]
	s_waitcnt vmcnt(31)
	v_cvt_pk_bf16_f32 v6, v6, v7
	v_cvt_pk_bf16_f32 v7, v8, v9
	s_waitcnt lgkmcnt(0)
	v_mfma_f32_16x16x32_bf16 v[134:137], v[152:155], v[144:147], v[134:137]
	ds_read_b128 v[138:141], v157
	v_lshl_or_b32 v144, v156, 8, v204
	ds_read_b128 v[144:147], v144
	v_or_b32_e32 v156, 2, v143
	s_waitcnt lgkmcnt(1)
	v_mfma_f32_16x16x32_bf16 v[2:5], v[138:141], v[148:151], v[2:5]
	v_lshl_or_b32 v138, v156, 10, v198
	ds_read_b128 v[138:141], v138
	ds_read_b128 v[152:155], v221
	s_waitcnt lgkmcnt(2)
	v_mfma_f32_16x16x32_bf16 v[134:137], v[144:147], v[148:151], v[134:137]
	v_lshl_or_b32 v144, v156, 8, v204
	v_or_b32_e32 v156, 3, v143
	ds_read_b128 v[144:147], v144
	ds_read_b128 v[148:151], v219
	s_waitcnt lgkmcnt(2)
	v_mfma_f32_16x16x32_bf16 v[2:5], v[138:141], v[152:155], v[2:5]
	v_lshl_or_b32 v138, v156, 10, v198
	ds_read_b128 v[138:141], v138
	s_waitcnt lgkmcnt(2)
	v_mfma_f32_16x16x32_bf16 v[134:137], v[144:147], v[152:155], v[134:137]
	v_lshl_or_b32 v144, v156, 8, v204
	ds_read_b128 v[144:147], v144
	v_or_b32_e32 v152, 4, v143
	s_waitcnt lgkmcnt(1)
	v_mfma_f32_16x16x32_bf16 v[2:5], v[138:141], v[148:151], v[2:5]
	v_lshl_or_b32 v138, v152, 10, v198
	ds_read_b128 v[138:141], v138
	v_or_b32_e32 v156, 5, v143
	s_waitcnt lgkmcnt(1)
	v_mfma_f32_16x16x32_bf16 v[134:137], v[144:147], v[148:151], v[134:137]
	ds_read_b128 v[144:147], v218
	v_lshl_or_b32 v148, v152, 8, v204
	ds_read_b128 v[148:151], v148
	ds_read_b128 v[152:155], v217
	s_waitcnt lgkmcnt(2)
	v_mfma_f32_16x16x32_bf16 v[2:5], v[138:141], v[144:147], v[2:5]
	v_lshl_or_b32 v138, v156, 10, v198
	ds_read_b128 v[138:141], v138
	s_waitcnt lgkmcnt(2)
	v_mfma_f32_16x16x32_bf16 v[134:137], v[148:151], v[144:147], v[134:137]
	v_lshl_or_b32 v144, v156, 8, v204
	ds_read_b128 v[144:147], v144
	v_or_b32_e32 v148, 6, v143
	s_waitcnt lgkmcnt(1)
	v_mfma_f32_16x16x32_bf16 v[2:5], v[138:141], v[152:155], v[2:5]
	v_lshl_or_b32 v138, v148, 10, v198
	ds_read_b128 v[138:141], v138
	v_lshl_or_b32 v148, v148, 8, v204
	s_waitcnt lgkmcnt(1)
	v_mfma_f32_16x16x32_bf16 v[134:137], v[144:147], v[152:155], v[134:137]
	ds_read_b128 v[144:147], v216
	ds_read_b128 v[148:151], v148
	ds_read_b128 v[152:155], v213
	v_or_b32_e32 v143, 7, v143
	ds_write_b64 v212, v[6:7]
	s_waitcnt lgkmcnt(3)
	v_mfma_f32_16x16x32_bf16 v[2:5], v[138:141], v[144:147], v[2:5]
	v_lshl_or_b32 v138, v143, 10, v198
	v_lshl_or_b32 v143, v143, 8, v204
	s_waitcnt vmcnt(19)
	v_cvt_pk_bf16_f32 v6, v18, v19
	v_cvt_pk_bf16_f32 v7, v20, v21
	ds_read_b128 v[138:141], v138
	s_waitcnt lgkmcnt(3)
	v_mfma_f32_16x16x32_bf16 v[134:137], v[148:151], v[144:147], v[134:137]
	ds_read_b128 v[144:147], v143
	ds_write_b64 v211, v[6:7] offset:512
	s_waitcnt vmcnt(18)
	v_cvt_pk_bf16_f32 v6, v26, v27
	v_cvt_pk_bf16_f32 v7, v28, v29
	ds_write_b64 v210, v[6:7] offset:1024
	s_waitcnt vmcnt(17)
	v_cvt_pk_bf16_f32 v6, v34, v35
	v_cvt_pk_bf16_f32 v7, v36, v37
	ds_write_b64 v209, v[6:7] offset:1536
	s_waitcnt vmcnt(16)
	v_cvt_pk_bf16_f32 v6, v42, v43
	v_cvt_pk_bf16_f32 v7, v44, v45
	ds_write_b64 v208, v[6:7] offset:2048
	v_cvt_pk_bf16_f32 v6, v50, v51
	v_cvt_pk_bf16_f32 v7, v52, v53
	ds_write_b64 v207, v[6:7] offset:2560
	v_cvt_pk_bf16_f32 v6, v58, v59
	v_cvt_pk_bf16_f32 v7, v60, v61
	ds_write_b64 v206, v[6:7] offset:3072
	v_cvt_pk_bf16_f32 v6, v66, v67
	v_cvt_pk_bf16_f32 v7, v68, v69
	ds_write_b64 v205, v[6:7] offset:3584
	v_cvt_pk_bf16_f32 v6, v74, v75
	v_cvt_pk_bf16_f32 v7, v76, v77
	ds_write_b64 v231, v[6:7] offset:4096
	v_cvt_pk_bf16_f32 v6, v82, v83
	v_cvt_pk_bf16_f32 v7, v84, v85
	ds_write_b64 v230, v[6:7] offset:4608
	v_cvt_pk_bf16_f32 v6, v90, v91
	v_cvt_pk_bf16_f32 v7, v92, v93
	s_waitcnt lgkmcnt(9)
	v_mfma_f32_16x16x32_bf16 v[134:137], v[144:147], v[152:155], v[134:137]
	ds_write_b64 v229, v[6:7] offset:5120
	v_cvt_pk_bf16_f32 v6, v98, v99
	v_cvt_pk_bf16_f32 v7, v100, v101
	ds_write_b64 v228, v[6:7] offset:5632
	v_cvt_pk_bf16_f32 v6, v102, v103
	v_cvt_pk_bf16_f32 v7, v104, v105
	ds_write_b64 v227, v[6:7] offset:6144
	v_cvt_pk_bf16_f32 v6, v110, v111
	v_cvt_pk_bf16_f32 v7, v112, v113
	ds_write_b64 v226, v[6:7] offset:6656
	v_cvt_pk_bf16_f32 v6, v118, v119
	v_cvt_pk_bf16_f32 v7, v120, v121
	v_mfma_f32_16x16x32_bf16 v[2:5], v[138:141], v[152:155], v[2:5]
	ds_write_b64 v225, v[6:7] offset:7168
	v_cvt_pk_bf16_f32 v6, v126, v127
	v_cvt_pk_bf16_f32 v7, v128, v129
	ds_write_b64 v224, v[6:7] offset:7680
	v_add_u32_e32 v6, 48, v232
	v_and_b32_e32 v50, 56, v6
	v_lshl_or_b32 v6, v50, 10, v198
	v_lshl_or_b32 v34, v50, 8, v204
	ds_read_b128 v[6:9], v6
	ds_read_b128 v[18:21], v223
	ds_read_b128 v[26:29], v222
	ds_read_b128 v[34:37], v34
	v_or_b32_e32 v42, 1, v50
	v_lshl_or_b32 v43, v42, 10, v198
	s_waitcnt lgkmcnt(2)
	v_mfma_f32_16x16x32_bf16 v[2:5], v[6:9], v[18:21], v[2:5]
	ds_read_b128 v[6:9], v43
	v_or_b32_e32 v51, 2, v50
	s_waitcnt lgkmcnt(1)
	v_mfma_f32_16x16x32_bf16 v[18:21], v[34:37], v[18:21], v[134:137]
	v_lshl_or_b32 v34, v42, 8, v204
	ds_read_b128 v[34:37], v34
	s_waitcnt lgkmcnt(1)
	v_mfma_f32_16x16x32_bf16 v[2:5], v[6:9], v[26:29], v[2:5]
	v_lshl_or_b32 v6, v51, 10, v198
	ds_read_b128 v[6:9], v6
	ds_read_b128 v[42:45], v221
	s_waitcnt lgkmcnt(2)
	v_mfma_f32_16x16x32_bf16 v[18:21], v[34:37], v[26:29], v[18:21]
	v_lshl_or_b32 v26, v51, 8, v204
	v_or_b32_e32 v51, 3, v50
	ds_read_b128 v[26:29], v26
	ds_read_b128 v[34:37], v219
	s_waitcnt lgkmcnt(2)
	v_mfma_f32_16x16x32_bf16 v[2:5], v[6:9], v[42:45], v[2:5]
	v_lshl_or_b32 v6, v51, 10, v198
	ds_read_b128 v[6:9], v6
	s_waitcnt lgkmcnt(2)
	v_mfma_f32_16x16x32_bf16 v[18:21], v[26:29], v[42:45], v[18:21]
	v_lshl_or_b32 v26, v51, 8, v204
	ds_read_b128 v[26:29], v26
	v_or_b32_e32 v42, 4, v50
	s_waitcnt lgkmcnt(1)
	v_mfma_f32_16x16x32_bf16 v[2:5], v[6:9], v[34:37], v[2:5]
	v_lshl_or_b32 v6, v42, 10, v198
	ds_read_b128 v[6:9], v6
	v_or_b32_e32 v51, 5, v50
	s_waitcnt lgkmcnt(1)
	v_mfma_f32_16x16x32_bf16 v[18:21], v[26:29], v[34:37], v[18:21]
	ds_read_b128 v[26:29], v218
	v_lshl_or_b32 v34, v42, 8, v204
	ds_read_b128 v[34:37], v34
	ds_read_b128 v[42:45], v217
	s_waitcnt lgkmcnt(2)
	v_mfma_f32_16x16x32_bf16 v[2:5], v[6:9], v[26:29], v[2:5]
	v_lshl_or_b32 v6, v51, 10, v198
	ds_read_b128 v[6:9], v6
	s_waitcnt lgkmcnt(2)
	v_mfma_f32_16x16x32_bf16 v[18:21], v[34:37], v[26:29], v[18:21]
	v_lshl_or_b32 v26, v51, 8, v204
	ds_read_b128 v[26:29], v26
	v_or_b32_e32 v34, 6, v50
	s_waitcnt lgkmcnt(1)
	v_mfma_f32_16x16x32_bf16 v[2:5], v[6:9], v[42:45], v[2:5]
	v_lshl_or_b32 v6, v34, 10, v198
	ds_read_b128 v[6:9], v6
	v_lshl_or_b32 v34, v34, 8, v204
	s_waitcnt lgkmcnt(1)
	v_mfma_f32_16x16x32_bf16 v[18:21], v[26:29], v[42:45], v[18:21]
	ds_read_b128 v[26:29], v216
	ds_read_b128 v[34:37], v34
	ds_read_b128 v[42:45], v213
	v_or_b32_e32 v50, 7, v50
	s_waitcnt lgkmcnt(2)
	v_mfma_f32_16x16x32_bf16 v[2:5], v[6:9], v[26:29], v[2:5]
	v_lshl_or_b32 v6, v50, 10, v198
	ds_read_b128 v[6:9], v6
	s_waitcnt lgkmcnt(2)
	v_mfma_f32_16x16x32_bf16 v[18:21], v[34:37], v[26:29], v[18:21]
	v_lshl_or_b32 v26, v50, 8, v204
	ds_read_b128 v[26:29], v26
	s_waitcnt lgkmcnt(1)
	v_mfma_f32_16x16x32_bf16 v[34:37], v[6:9], v[42:45], v[2:5]
	v_and_b32_e32 v74, 7, v197
	v_lshrrev_b32_e32 v75, 3, v197
	v_lshlrev_b32_e32 v192, 13, v200
	v_lshlrev_b32_e32 v193, 11, v200
	v_lshl_add_u32 v203, v197, 2, v196
	v_lshl_or_b32 v192, v75, 8, v192
	v_lshl_or_b32 v193, v75, 6, v193
	v_add_u32_e32 v203, 0x24800, v203
	v_lshl_or_b32 v192, v201, 6, v192
	v_lshl_or_b32 v193, v74, 1, v193
	v_lshl_or_b32 v192, v74, 1, v192
	v_or_b32_e32 v193, 0x10000, v193
	v_cmp_gt_u32_e64 s[36:37], 16, v1
	v_cmp_eq_u32_e64 s[38:39], 1, v201
	ds_read2_b32 v[2:3], v203 offset1:16
	ds_read2_b32 v[4:5], v203 offset0:32 offset1:48
	ds_read2_b32 v[6:7], v203 offset0:64 offset1:80
	ds_read2_b32 v[8:9], v203 offset0:96 offset1:112
	ds_read2_b32 v[50:51], v203 offset0:128 offset1:144
	ds_read2_b32 v[52:53], v203 offset0:160 offset1:176
	ds_read2_b32 v[58:59], v203 offset0:192 offset1:208
	ds_read2_b32 v[60:61], v203 offset0:224 offset1:240
	v_mov_b32_e32 v146, 0
	v_mov_b32_e32 v147, 0
	v_mov_b32_e32 v150, 0
	v_mov_b32_e32 v151, 0
	v_mov_b32_e32 v154, 0
	v_mov_b32_e32 v155, 0
	v_mov_b32_e32 v158, 0
	v_mov_b32_e32 v159, 0
	v_mov_b32_e32 v162, 0
	v_mov_b32_e32 v163, 0
	v_mov_b32_e32 v166, 0
	v_mov_b32_e32 v167, 0
	v_mov_b32_e32 v170, 0
	v_mov_b32_e32 v171, 0
	v_mov_b32_e32 v174, 0
	v_mov_b32_e32 v175, 0
	v_mov_b32_e32 v178, 0
	v_mov_b32_e32 v179, 0
	v_mov_b32_e32 v182, 0
	v_mov_b32_e32 v183, 0
	v_mov_b32_e32 v186, 0
	v_mov_b32_e32 v187, 0
	v_mov_b32_e32 v190, 0
	v_mov_b32_e32 v191, 0
	v_mov_b32_e32 v234, 0
	v_mov_b32_e32 v235, 0
	v_mov_b32_e32 v238, 0
	v_mov_b32_e32 v239, 0
	v_mov_b32_e32 v242, 0
	v_mov_b32_e32 v243, 0
	v_mov_b32_e32 v246, 0
	v_mov_b32_e32 v247, 0
	ds_read_u16 v82, v192
	ds_read_u16 v83, v192 offset:16
	ds_read_u16 v84, v192 offset:32
	ds_read_u16 v85, v192 offset:48
	ds_read_u16 v90, v193
	ds_read_u16 v91, v193 offset:16
	ds_read_u16 v92, v193 offset:32
	ds_read_u16 v93, v193 offset:48
	ds_read_u16 v98, v192 offset:512
	ds_read_u16 v99, v192 offset:528
	ds_read_u16 v100, v192 offset:544
	ds_read_u16 v101, v192 offset:560
	ds_read_u16 v102, v193 offset:128
	ds_read_u16 v103, v193 offset:144
	ds_read_u16 v104, v193 offset:160
	ds_read_u16 v105, v193 offset:176
	s_waitcnt lgkmcnt(8)
	v_lshl_or_b32 v144, v83, 16, v82
	v_lshl_or_b32 v145, v85, 16, v84
	s_mov_b64 exec, s[36:37]
	v_lshl_or_b32 v146, v91, 16, v90
	v_lshl_or_b32 v147, v93, 16, v92
	s_mov_b64 exec, -1
	ds_read_u16 v82, v192 offset:1024
	ds_read_u16 v83, v192 offset:1040
	ds_read_u16 v84, v192 offset:1056
	ds_read_u16 v85, v192 offset:1072
	ds_read_u16 v90, v193 offset:256
	ds_read_u16 v91, v193 offset:272
	ds_read_u16 v92, v193 offset:288
	ds_read_u16 v93, v193 offset:304
	s_waitcnt lgkmcnt(8)
	v_lshl_or_b32 v148, v99, 16, v98
	v_lshl_or_b32 v149, v101, 16, v100
	s_mov_b64 exec, s[36:37]
	v_lshl_or_b32 v150, v103, 16, v102
	v_lshl_or_b32 v151, v105, 16, v104
	s_mov_b64 exec, -1
	ds_read_u16 v98, v192 offset:1536
	ds_read_u16 v99, v192 offset:1552
	ds_read_u16 v100, v192 offset:1568
	ds_read_u16 v101, v192 offset:1584
	ds_read_u16 v102, v193 offset:384
	ds_read_u16 v103, v193 offset:400
	ds_read_u16 v104, v193 offset:416
	ds_read_u16 v105, v193 offset:432
	s_waitcnt lgkmcnt(8)
	v_lshl_or_b32 v152, v83, 16, v82
	v_lshl_or_b32 v153, v85, 16, v84
	s_mov_b64 exec, s[36:37]
	v_lshl_or_b32 v154, v91, 16, v90
	v_lshl_or_b32 v155, v93, 16, v92
	s_mov_b64 exec, -1
	ds_read_u16 v82, v192 offset:2048
	ds_read_u16 v83, v192 offset:2064
	ds_read_u16 v84, v192 offset:2080
	ds_read_u16 v85, v192 offset:2096
	ds_read_u16 v90, v193 offset:512
	ds_read_u16 v91, v193 offset:528
	ds_read_u16 v92, v193 offset:544
	ds_read_u16 v93, v193 offset:560
	s_waitcnt lgkmcnt(8)
	v_lshl_or_b32 v156, v99, 16, v98
	v_lshl_or_b32 v157, v101, 16, v100
	s_mov_b64 exec, s[36:37]
	v_lshl_or_b32 v158, v103, 16, v102
	v_lshl_or_b32 v159, v105, 16, v104
	s_mov_b64 exec, -1
	ds_read_u16 v98, v192 offset:2560
	ds_read_u16 v99, v192 offset:2576
	ds_read_u16 v100, v192 offset:2592
	ds_read_u16 v101, v192 offset:2608
	ds_read_u16 v102, v193 offset:640
	ds_read_u16 v103, v193 offset:656
	ds_read_u16 v104, v193 offset:672
	ds_read_u16 v105, v193 offset:688
	s_waitcnt lgkmcnt(8)
	v_lshl_or_b32 v160, v83, 16, v82
	v_lshl_or_b32 v161, v85, 16, v84
	s_mov_b64 exec, s[36:37]
	v_lshl_or_b32 v162, v91, 16, v90
	v_lshl_or_b32 v163, v93, 16, v92
	s_mov_b64 exec, -1
	ds_read_u16 v82, v192 offset:3072
	ds_read_u16 v83, v192 offset:3088
	ds_read_u16 v84, v192 offset:3104
	ds_read_u16 v85, v192 offset:3120
	ds_read_u16 v90, v193 offset:768
	ds_read_u16 v91, v193 offset:784
	ds_read_u16 v92, v193 offset:800
	ds_read_u16 v93, v193 offset:816
	s_waitcnt lgkmcnt(8)
	v_lshl_or_b32 v164, v99, 16, v98
	v_lshl_or_b32 v165, v101, 16, v100
	s_mov_b64 exec, s[36:37]
	v_lshl_or_b32 v166, v103, 16, v102
	v_lshl_or_b32 v167, v105, 16, v104
	s_mov_b64 exec, -1
	ds_read_u16 v98, v192 offset:3584
	ds_read_u16 v99, v192 offset:3600
	ds_read_u16 v100, v192 offset:3616
	ds_read_u16 v101, v192 offset:3632
	ds_read_u16 v102, v193 offset:896
	ds_read_u16 v103, v193 offset:912
	ds_read_u16 v104, v193 offset:928
	ds_read_u16 v105, v193 offset:944
	s_waitcnt lgkmcnt(8)
	v_lshl_or_b32 v168, v83, 16, v82
	v_lshl_or_b32 v169, v85, 16, v84
	s_mov_b64 exec, s[36:37]
	v_lshl_or_b32 v170, v91, 16, v90
	v_lshl_or_b32 v171, v93, 16, v92
	s_mov_b64 exec, -1
	ds_read_u16 v82, v192 offset:4096
	ds_read_u16 v83, v192 offset:4112
	ds_read_u16 v84, v192 offset:4128
	ds_read_u16 v85, v192 offset:4144
	ds_read_u16 v90, v193 offset:1024
	ds_read_u16 v91, v193 offset:1040
	ds_read_u16 v92, v193 offset:1056
	ds_read_u16 v93, v193 offset:1072
	s_waitcnt lgkmcnt(8)
	v_lshl_or_b32 v172, v99, 16, v98
	v_lshl_or_b32 v173, v101, 16, v100
	s_mov_b64 exec, s[36:37]
	v_lshl_or_b32 v174, v103, 16, v102
	v_lshl_or_b32 v175, v105, 16, v104
	s_mov_b64 exec, -1
	ds_read_u16 v98, v192 offset:4608
	ds_read_u16 v99, v192 offset:4624
	ds_read_u16 v100, v192 offset:4640
	ds_read_u16 v101, v192 offset:4656
	ds_read_u16 v102, v193 offset:1152
	ds_read_u16 v103, v193 offset:1168
	ds_read_u16 v104, v193 offset:1184
	ds_read_u16 v105, v193 offset:1200
	s_waitcnt lgkmcnt(8)
	v_lshl_or_b32 v176, v83, 16, v82
	v_lshl_or_b32 v177, v85, 16, v84
	s_mov_b64 exec, s[36:37]
	v_lshl_or_b32 v178, v91, 16, v90
	v_lshl_or_b32 v179, v93, 16, v92
	s_mov_b64 exec, -1
	ds_read_u16 v82, v192 offset:5120
	ds_read_u16 v83, v192 offset:5136
	ds_read_u16 v84, v192 offset:5152
	ds_read_u16 v85, v192 offset:5168
	ds_read_u16 v90, v193 offset:1280
	ds_read_u16 v91, v193 offset:1296
	ds_read_u16 v92, v193 offset:1312
	ds_read_u16 v93, v193 offset:1328
	s_waitcnt lgkmcnt(8)
	v_lshl_or_b32 v180, v99, 16, v98
	v_lshl_or_b32 v181, v101, 16, v100
	s_mov_b64 exec, s[36:37]
	v_lshl_or_b32 v182, v103, 16, v102
	v_lshl_or_b32 v183, v105, 16, v104
	s_mov_b64 exec, -1
	ds_read_u16 v98, v192 offset:5632
	ds_read_u16 v99, v192 offset:5648
	ds_read_u16 v100, v192 offset:5664
	ds_read_u16 v101, v192 offset:5680
	ds_read_u16 v102, v193 offset:1408
	ds_read_u16 v103, v193 offset:1424
	ds_read_u16 v104, v193 offset:1440
	ds_read_u16 v105, v193 offset:1456
	s_waitcnt lgkmcnt(8)
	v_lshl_or_b32 v184, v83, 16, v82
	v_lshl_or_b32 v185, v85, 16, v84
	s_mov_b64 exec, s[36:37]
	v_lshl_or_b32 v186, v91, 16, v90
	v_lshl_or_b32 v187, v93, 16, v92
	s_mov_b64 exec, -1
	ds_read_u16 v82, v192 offset:6144
	ds_read_u16 v83, v192 offset:6160
	ds_read_u16 v84, v192 offset:6176
	ds_read_u16 v85, v192 offset:6192
	ds_read_u16 v90, v193 offset:1536
	ds_read_u16 v91, v193 offset:1552
	ds_read_u16 v92, v193 offset:1568
	ds_read_u16 v93, v193 offset:1584
	s_waitcnt lgkmcnt(8)
	v_lshl_or_b32 v188, v99, 16, v98
	v_lshl_or_b32 v189, v101, 16, v100
	s_mov_b64 exec, s[36:37]
	v_lshl_or_b32 v190, v103, 16, v102
	v_lshl_or_b32 v191, v105, 16, v104
	s_mov_b64 exec, -1
	ds_read_u16 v98, v192 offset:6656
	ds_read_u16 v99, v192 offset:6672
	ds_read_u16 v100, v192 offset:6688
	ds_read_u16 v101, v192 offset:6704
	ds_read_u16 v102, v193 offset:1664
	ds_read_u16 v103, v193 offset:1680
	ds_read_u16 v104, v193 offset:1696
	ds_read_u16 v105, v193 offset:1712
	s_waitcnt lgkmcnt(8)
	v_lshl_or_b32 v232, v83, 16, v82
	v_lshl_or_b32 v233, v85, 16, v84
	s_mov_b64 exec, s[36:37]
	v_lshl_or_b32 v234, v91, 16, v90
	v_lshl_or_b32 v235, v93, 16, v92
	s_mov_b64 exec, -1
	ds_read_u16 v82, v192 offset:7168
	ds_read_u16 v83, v192 offset:7184
	ds_read_u16 v84, v192 offset:7200
	ds_read_u16 v85, v192 offset:7216
	ds_read_u16 v90, v193 offset:1792
	ds_read_u16 v91, v193 offset:1808
	ds_read_u16 v92, v193 offset:1824
	ds_read_u16 v93, v193 offset:1840
	s_waitcnt lgkmcnt(8)
	v_lshl_or_b32 v236, v99, 16, v98
	v_lshl_or_b32 v237, v101, 16, v100
	s_mov_b64 exec, s[36:37]
	v_lshl_or_b32 v238, v103, 16, v102
	v_lshl_or_b32 v239, v105, 16, v104
	s_mov_b64 exec, -1
	ds_read_u16 v98, v192 offset:7680
	ds_read_u16 v99, v192 offset:7696
	ds_read_u16 v100, v192 offset:7712
	ds_read_u16 v101, v192 offset:7728
	ds_read_u16 v102, v193 offset:1920
	ds_read_u16 v103, v193 offset:1936
	ds_read_u16 v104, v193 offset:1952
	ds_read_u16 v105, v193 offset:1968
	s_waitcnt lgkmcnt(8)
	v_lshl_or_b32 v240, v83, 16, v82
	v_lshl_or_b32 v241, v85, 16, v84
	s_mov_b64 exec, s[36:37]
	v_lshl_or_b32 v242, v91, 16, v90
	v_lshl_or_b32 v243, v93, 16, v92
	s_mov_b64 exec, -1
	s_waitcnt lgkmcnt(0)
	v_lshl_or_b32 v244, v99, 16, v98
	v_lshl_or_b32 v245, v101, 16, v100
	s_mov_b64 exec, s[36:37]
	v_lshl_or_b32 v246, v103, 16, v102
	v_lshl_or_b32 v247, v105, 16, v104
	s_mov_b64 exec, -1
	s_waitcnt lgkmcnt(0)
	s_mov_b64 exec, s[38:39]
	v_cvt_pk_bf16_f32 v66, v2, v195
	v_cvt_pk_bf16_f32 v74, v3, v195
	v_lshlrev_b32_e32 v67, 16, v66
	v_lshlrev_b32_e32 v75, 16, v74
	v_sub_f32_e32 v2, v2, v67
	v_sub_f32_e32 v3, v3, v75
	v_cvt_pk_bf16_f32 v68, v2, v195
	v_cvt_pk_bf16_f32 v76, v3, v195
	v_lshlrev_b32_e32 v69, 16, v68
	v_lshlrev_b32_e32 v77, 16, v76
	v_sub_f32_e32 v2, v2, v69
	v_sub_f32_e32 v3, v3, v77
	v_cvt_pk_bf16_f32 v147, v2, v195
	v_cvt_pk_bf16_f32 v151, v3, v195
	v_cvt_pk_bf16_f32 v146, v67, v69
	v_cvt_pk_bf16_f32 v150, v75, v77
	v_cvt_pk_bf16_f32 v66, v4, v195
	v_cvt_pk_bf16_f32 v74, v5, v195
	v_lshlrev_b32_e32 v67, 16, v66
	v_lshlrev_b32_e32 v75, 16, v74
	v_sub_f32_e32 v4, v4, v67
	v_sub_f32_e32 v5, v5, v75
	v_cvt_pk_bf16_f32 v68, v4, v195
	v_cvt_pk_bf16_f32 v76, v5, v195
	v_lshlrev_b32_e32 v69, 16, v68
	v_lshlrev_b32_e32 v77, 16, v76
	v_sub_f32_e32 v4, v4, v69
	v_sub_f32_e32 v5, v5, v77
	v_cvt_pk_bf16_f32 v155, v4, v195
	v_cvt_pk_bf16_f32 v159, v5, v195
	v_cvt_pk_bf16_f32 v154, v67, v69
	v_cvt_pk_bf16_f32 v158, v75, v77
	v_cvt_pk_bf16_f32 v66, v6, v195
	v_cvt_pk_bf16_f32 v74, v7, v195
	v_lshlrev_b32_e32 v67, 16, v66
	v_lshlrev_b32_e32 v75, 16, v74
	v_sub_f32_e32 v6, v6, v67
	v_sub_f32_e32 v7, v7, v75
	v_cvt_pk_bf16_f32 v68, v6, v195
	v_cvt_pk_bf16_f32 v76, v7, v195
	v_lshlrev_b32_e32 v69, 16, v68
	v_lshlrev_b32_e32 v77, 16, v76
	v_sub_f32_e32 v6, v6, v69
	v_sub_f32_e32 v7, v7, v77
	v_cvt_pk_bf16_f32 v163, v6, v195
	v_cvt_pk_bf16_f32 v167, v7, v195
	v_cvt_pk_bf16_f32 v162, v67, v69
	v_cvt_pk_bf16_f32 v166, v75, v77
	v_cvt_pk_bf16_f32 v66, v8, v195
	v_cvt_pk_bf16_f32 v74, v9, v195
	v_lshlrev_b32_e32 v67, 16, v66
	v_lshlrev_b32_e32 v75, 16, v74
	v_sub_f32_e32 v8, v8, v67
	v_sub_f32_e32 v9, v9, v75
	v_cvt_pk_bf16_f32 v68, v8, v195
	v_cvt_pk_bf16_f32 v76, v9, v195
	v_lshlrev_b32_e32 v69, 16, v68
	v_lshlrev_b32_e32 v77, 16, v76
	v_sub_f32_e32 v8, v8, v69
	v_sub_f32_e32 v9, v9, v77
	v_cvt_pk_bf16_f32 v171, v8, v195
	v_cvt_pk_bf16_f32 v175, v9, v195
	v_cvt_pk_bf16_f32 v170, v67, v69
	v_cvt_pk_bf16_f32 v174, v75, v77
	v_cvt_pk_bf16_f32 v66, v50, v195
	v_cvt_pk_bf16_f32 v74, v51, v195
	v_lshlrev_b32_e32 v67, 16, v66
	v_lshlrev_b32_e32 v75, 16, v74
	v_sub_f32_e32 v50, v50, v67
	v_sub_f32_e32 v51, v51, v75
	v_cvt_pk_bf16_f32 v68, v50, v195
	v_cvt_pk_bf16_f32 v76, v51, v195
	v_lshlrev_b32_e32 v69, 16, v68
	v_lshlrev_b32_e32 v77, 16, v76
	v_sub_f32_e32 v50, v50, v69
	v_sub_f32_e32 v51, v51, v77
	v_cvt_pk_bf16_f32 v179, v50, v195
	v_cvt_pk_bf16_f32 v183, v51, v195
	v_cvt_pk_bf16_f32 v178, v67, v69
	v_cvt_pk_bf16_f32 v182, v75, v77
	v_cvt_pk_bf16_f32 v66, v52, v195
	v_cvt_pk_bf16_f32 v74, v53, v195
	v_lshlrev_b32_e32 v67, 16, v66
	v_lshlrev_b32_e32 v75, 16, v74
	v_sub_f32_e32 v52, v52, v67
	v_sub_f32_e32 v53, v53, v75
	v_cvt_pk_bf16_f32 v68, v52, v195
	v_cvt_pk_bf16_f32 v76, v53, v195
	v_lshlrev_b32_e32 v69, 16, v68
	v_lshlrev_b32_e32 v77, 16, v76
	v_sub_f32_e32 v52, v52, v69
	v_sub_f32_e32 v53, v53, v77
	v_cvt_pk_bf16_f32 v187, v52, v195
	v_cvt_pk_bf16_f32 v191, v53, v195
	v_cvt_pk_bf16_f32 v186, v67, v69
	v_cvt_pk_bf16_f32 v190, v75, v77
	v_cvt_pk_bf16_f32 v66, v58, v195
	v_cvt_pk_bf16_f32 v74, v59, v195
	v_lshlrev_b32_e32 v67, 16, v66
	v_lshlrev_b32_e32 v75, 16, v74
	v_sub_f32_e32 v58, v58, v67
	v_sub_f32_e32 v59, v59, v75
	v_cvt_pk_bf16_f32 v68, v58, v195
	v_cvt_pk_bf16_f32 v76, v59, v195
	v_lshlrev_b32_e32 v69, 16, v68
	v_lshlrev_b32_e32 v77, 16, v76
	v_sub_f32_e32 v58, v58, v69
	v_sub_f32_e32 v59, v59, v77
	v_cvt_pk_bf16_f32 v235, v58, v195
	v_cvt_pk_bf16_f32 v239, v59, v195
	v_cvt_pk_bf16_f32 v234, v67, v69
	v_cvt_pk_bf16_f32 v238, v75, v77
	v_cvt_pk_bf16_f32 v66, v60, v195
	v_cvt_pk_bf16_f32 v74, v61, v195
	v_lshlrev_b32_e32 v67, 16, v66
	v_lshlrev_b32_e32 v75, 16, v74
	v_sub_f32_e32 v60, v60, v67
	v_sub_f32_e32 v61, v61, v75
	v_cvt_pk_bf16_f32 v68, v60, v195
	v_cvt_pk_bf16_f32 v76, v61, v195
	v_lshlrev_b32_e32 v69, 16, v68
	v_lshlrev_b32_e32 v77, 16, v76
	v_sub_f32_e32 v60, v60, v69
	v_sub_f32_e32 v61, v61, v77
	v_cvt_pk_bf16_f32 v243, v60, v195
	v_cvt_pk_bf16_f32 v247, v61, v195
	v_cvt_pk_bf16_f32 v242, v67, v69
	v_cvt_pk_bf16_f32 v246, v75, v77
	s_mov_b64 exec, -1
	s_waitcnt vmcnt(15)
	v_cvt_pk_bf16_f32 v6, v10, v11
	v_cvt_pk_bf16_f32 v7, v12, v13
	ds_write_b64 v212, v[6:7]
	s_waitcnt vmcnt(14)
	v_cvt_pk_bf16_f32 v6, v14, v15
	v_cvt_pk_bf16_f32 v7, v16, v17
	ds_write_b64 v211, v[6:7] offset:512
	s_waitcnt vmcnt(13)
	v_cvt_pk_bf16_f32 v6, v22, v23
	v_cvt_pk_bf16_f32 v7, v24, v25
	ds_write_b64 v210, v[6:7] offset:1024
	s_waitcnt vmcnt(12)
	v_cvt_pk_bf16_f32 v6, v30, v31
	v_cvt_pk_bf16_f32 v7, v32, v33
	ds_write_b64 v209, v[6:7] offset:1536
	s_waitcnt vmcnt(11)
	v_cvt_pk_bf16_f32 v6, v38, v39
	v_cvt_pk_bf16_f32 v7, v40, v41
	ds_write_b64 v208, v[6:7] offset:2048
	s_waitcnt vmcnt(10)
	v_cvt_pk_bf16_f32 v6, v46, v47
	v_cvt_pk_bf16_f32 v7, v48, v49
	ds_write_b64 v207, v[6:7] offset:2560
	s_waitcnt vmcnt(9)
	v_cvt_pk_bf16_f32 v6, v54, v55
	v_cvt_pk_bf16_f32 v7, v56, v57
	ds_write_b64 v206, v[6:7] offset:3072
	s_waitcnt vmcnt(8)
	v_cvt_pk_bf16_f32 v6, v62, v63
	v_cvt_pk_bf16_f32 v7, v64, v65
	ds_write_b64 v205, v[6:7] offset:3584
	s_waitcnt vmcnt(7)
	v_cvt_pk_bf16_f32 v6, v70, v71
	v_cvt_pk_bf16_f32 v7, v72, v73
	ds_write_b64 v231, v[6:7] offset:4096
	s_waitcnt vmcnt(6)
	v_cvt_pk_bf16_f32 v6, v78, v79
	v_cvt_pk_bf16_f32 v7, v80, v81
	ds_write_b64 v230, v[6:7] offset:4608
	s_waitcnt vmcnt(5)
	v_cvt_pk_bf16_f32 v6, v86, v87
	v_cvt_pk_bf16_f32 v7, v88, v89
	ds_write_b64 v229, v[6:7] offset:5120
	s_waitcnt vmcnt(4)
	v_cvt_pk_bf16_f32 v6, v94, v95
	v_cvt_pk_bf16_f32 v7, v96, v97
	ds_write_b64 v228, v[6:7] offset:5632
	s_waitcnt vmcnt(3)
	v_cvt_pk_bf16_f32 v6, v106, v107
	v_cvt_pk_bf16_f32 v7, v108, v109
	ds_write_b64 v227, v[6:7] offset:6144
	s_waitcnt vmcnt(2)
	v_cvt_pk_bf16_f32 v6, v114, v115
	v_cvt_pk_bf16_f32 v7, v116, v117
	ds_write_b64 v226, v[6:7] offset:6656
	s_waitcnt vmcnt(1)
	v_cvt_pk_bf16_f32 v6, v122, v123
	v_cvt_pk_bf16_f32 v7, v124, v125
	s_waitcnt lgkmcnt(14)
	v_mfma_f32_16x16x32_bf16 v[2:5], v[26:29], v[42:45], v[18:21]
	ds_write_b64 v225, v[6:7] offset:7168
	s_waitcnt vmcnt(0)
	v_cvt_pk_bf16_f32 v6, v130, v131
	v_cvt_pk_bf16_f32 v7, v132, v133
	ds_write_b64 v224, v[6:7] offset:7680
	v_lshlrev_b32_e32 v6, 3, v142
	v_and_b32_e32 v58, 56, v6
	v_lshl_or_b32 v6, v58, 10, v198
	v_or_b32_e32 v18, 1, v58
	v_lshl_or_b32 v7, v58, 8, v204
	ds_read_b128 v[14:17], v6
	ds_read_b128 v[10:13], v7
	v_lshl_or_b32 v6, v18, 10, v198
	ds_read_b128 v[26:29], v6
	ds_read_b128 v[22:25], v223
	ds_read_b128 v[6:9], v222
	v_or_b32_e32 v42, 2, v58
	v_lshl_or_b32 v19, v42, 10, v198
	ds_read_b128 v[38:41], v19
	s_waitcnt lgkmcnt(2)
	v_mfma_f32_16x16x32_bf16 v[30:33], v[14:17], v[22:25], v[34:37]
	v_lshl_or_b32 v14, v18, 8, v204
	ds_read_b128 v[18:21], v14
	ds_read_b128 v[14:17], v221
	v_or_b32_e32 v59, 5, v58
	s_waitcnt lgkmcnt(3)
	v_mfma_f32_16x16x32_bf16 v[34:37], v[26:29], v[6:9], v[30:33]
	v_lshl_or_b32 v26, v42, 8, v204
	ds_read_b128 v[26:29], v26
	s_nop 0
	ds_read_b128 v[30:33], v219
	v_or_b32_e32 v68, 6, v58
	s_waitcnt lgkmcnt(2)
	v_mfma_f32_16x16x32_bf16 v[38:41], v[38:41], v[14:17], v[34:37]
	v_lshl_or_b32 v64, v68, 10, v198
	s_nop 1
	v_or_b32_e32 v34, 3, v58
	v_lshl_or_b32 v35, v34, 10, v198
	ds_read_b128 v[42:45], v35
	v_lshl_or_b32 v34, v34, 8, v204
	s_waitcnt lgkmcnt(0)
	v_mfma_f32_16x16x32_bf16 v[46:49], v[42:45], v[30:33], v[38:41]
	s_nop 2
	v_or_b32_e32 v38, 4, v58
	v_lshl_or_b32 v39, v38, 10, v198
	v_lshl_or_b32 v38, v38, 8, v204
	ds_read_b128 v[34:37], v34
	ds_read_b128 v[50:53], v39
	ds_read_b128 v[42:45], v38
	v_lshl_or_b32 v38, v59, 10, v198
	ds_read_b128 v[54:57], v38
	ds_read_b128 v[60:63], v218
	ds_read_b128 v[38:41], v217
	ds_read_b128 v[72:75], v64
	s_waitcnt lgkmcnt(2)
	v_mfma_f32_16x16x32_bf16 v[64:67], v[50:53], v[60:63], v[46:49]
	v_or_b32_e32 v58, 7, v58
	s_nop 1
	v_lshl_or_b32 v46, v59, 8, v204
	v_lshl_or_b32 v59, v68, 8, v204
	ds_read_b128 v[50:53], v46
	ds_read_b128 v[46:49], v216
	s_waitcnt lgkmcnt(3)
	v_mfma_f32_16x16x32_bf16 v[54:57], v[54:57], v[38:41], v[64:67]
	s_nop 2
	ds_read_b128 v[64:67], v59
	ds_read_b128 v[68:71], v213
	v_lshl_or_b32 v59, v58, 10, v198
	ds_read_b128 v[76:79], v59
	s_waitcnt lgkmcnt(3)
	v_mfma_f32_16x16x32_bf16 v[54:57], v[72:75], v[46:49], v[54:57]
	v_lshl_or_b32 v58, v58, 8, v204
	ds_read_b128 v[72:75], v58
	s_waitcnt lgkmcnt(1)
	v_mfma_f32_16x16x32_bf16 v[56:59], v[76:79], v[68:71], v[54:57]
	s_nop 2
	v_add_u32_e32 v76, 0x24800, v196
	s_waitcnt lgkmcnt(0)
	v_mfma_f32_16x16x32_bf16 v[2:5], v[10:13], v[22:25], v[2:5]
	v_mfma_f32_16x16x32_bf16 v[2:5], v[18:21], v[6:9], v[2:5]
	s_waitcnt lgkmcnt(0)
	v_mfma_f32_16x16x32_bf16 v[2:5], v[26:29], v[14:17], v[2:5]
	v_mfma_f32_16x16x32_bf16 v[2:5], v[34:37], v[30:33], v[2:5]
	s_waitcnt lgkmcnt(0)
	v_mfma_f32_16x16x32_bf16 v[2:5], v[42:45], v[60:63], v[2:5]
	v_mfma_f32_16x16x32_bf16 v[2:5], v[50:53], v[38:41], v[2:5]
	s_waitcnt lgkmcnt(0)
	v_mfma_f32_16x16x32_bf16 v[2:5], v[64:67], v[46:49], v[2:5]
	v_mfma_f32_16x16x32_bf16 v[60:63], v[72:75], v[68:71], v[2:5]
	s_waitcnt lgkmcnt(0)
	v_cmp_gt_u32_e64 s[0:1], 16, v1
	v_cmp_lt_u32_e32 vcc, 15, v1
	s_waitcnt lgkmcnt(0)
	s_nop 2
	v_max_f32_e32 v2, v59, v59
	v_max_f32_e32 v3, v58, v58
	s_waitcnt lgkmcnt(0)
	v_max_f32_e32 v2, v3, v2
	s_nop 0
	s_nop 0
	s_nop 0
	s_waitcnt lgkmcnt(0)
	s_nop 0
	s_nop 0
	s_and_saveexec_b64 s[4:5], vcc
	s_xor_b64 s[4:5], exec, s[4:5]
	s_or_saveexec_b64 s[4:5], s[4:5]
	v_max3_f32 v53, v56, v57, v2
	s_xor_b64 exec, exec, s[4:5]
	v_max_f32_e32 v2, v61, v61
	v_max_f32_e32 v3, v60, v60
	v_max_f32_e32 v2, v3, v2
	v_max_f32_e32 v3, v63, v63
	v_max_f32_e32 v4, v62, v62
	v_max_f32_e32 v3, v4, v3
	v_max3_f32 v53, v53, v2, v3
	s_or_b64 exec, exec, s[4:5]
	v_cmp_eq_u32_e64 s[4:5], 1, v201
	v_max_f32_e32 v53, v53, v53
	v_mov_b32_e32 v68, v53
	s_nop 1
	v_permlane16_swap_b32_e32 v53, v68
	v_max_f32_e32 v68, v53, v68
	v_mov_b32_e32 v55, v68
	s_nop 1
	v_permlane32_swap_b32_e32 v68, v55
	v_max_f32_e32 v68, v68, v55
	v_sub_f32_e32 v55, v56, v68
	v_mul_f32_e32 v55, 0x3fb8aa3b, v55
	v_exp_f32_e32 v70, v55
	v_sub_f32_e32 v55, v57, v68
	v_sub_f32_e32 v57, v59, v68
	v_mul_f32_e32 v57, 0x3fb8aa3b, v57
	v_mul_f32_e32 v55, 0x3fb8aa3b, v55
	v_exp_f32_e32 v59, v57
	v_sub_f32_e32 v57, v60, v68
	v_exp_f32_e32 v71, v55
	v_sub_f32_e32 v55, v58, v68
	v_mul_f32_e32 v57, 0x3fb8aa3b, v57
	v_sub_f32_e32 v58, v61, v68
	v_exp_f32_e32 v57, v57
	v_mul_f32_e32 v58, 0x3fb8aa3b, v58
	v_exp_f32_e32 v58, v58
	v_mul_f32_e32 v55, 0x3fb8aa3b, v55
	v_exp_f32_e32 v72, v55
	v_cndmask_b32_e64 v60, 0, v57, s[0:1]
	v_sub_f32_e32 v57, v62, v68
	v_add_f32_e32 v56, 0, v70
	v_cndmask_b32_e64 v61, 0, v58, s[0:1]
	v_mul_f32_e32 v57, 0x3fb8aa3b, v57
	v_sub_f32_e32 v58, v63, v68
	v_add_f32_e32 v56, v56, v71
	v_exp_f32_e32 v57, v57
	v_mul_f32_e32 v58, 0x3fb8aa3b, v58
	v_add_f32_e32 v56, v56, v72
	v_exp_f32_e32 v58, v58
	v_add_f32_e32 v56, v56, v59
	v_add_f32_e32 v56, v56, v60
	v_add_f32_e32 v56, v56, v61
	v_cndmask_b32_e64 v62, 0, v57, s[0:1]
	v_add_f32_e32 v56, v56, v62
	v_cndmask_b32_e64 v63, 0, v58, s[0:1]
	v_add_f32_e32 v57, v56, v63
	v_mov_b32_e32 v58, v57
	s_nop 1
	v_permlane16_swap_b32_e32 v57, v58
	v_add_f32_e32 v58, v57, v58
	v_mov_b32_e32 v68, v58
	s_nop 1
	v_permlane32_swap_b32_e32 v58, v68
	v_add_f32_e32 v68, v58, v68
	v_div_scale_f32 v69, s[6:7], v68, v68, 1.0
	v_rcp_f32_e32 v73, v69
	s_nop 0
	v_fma_f32 v75, -v69, v73, 1.0
	v_fmac_f32_e32 v73, v75, v73
	v_div_scale_f32 v75, vcc, 1.0, v68, 1.0
	v_mul_f32_e32 v92, v75, v73
	v_fma_f32 v93, -v69, v92, v75
	v_fmac_f32_e32 v92, v93, v73
	v_fma_f32 v69, -v69, v92, v75
	v_div_fmas_f32 v69, v69, v73, v92
	v_div_fixup_f32 v68, v69, v68, 1.0
	v_mul_f32_e32 v69, v68, v70
	v_mov_b32_e32 v75, 0xbb23d70a
	v_mov_b32_e32 v73, 0x3b23d70a
	v_fmaak_f32 v92, v68, v70, 0xbb23d70a
	v_fmaak_f32 v70, v68, v70, 0x3b23d70a
	v_cmp_lt_f32_e32 vcc, v69, v75
	v_fmaak_f32 v93, v68, v60, 0xbb23d70a
	s_nop 0
	v_cndmask_b32_e32 v70, 0, v70, vcc
	v_cmp_gt_f32_e32 vcc, v69, v73
	s_nop 1
	v_cndmask_b32_e32 v69, v70, v92, vcc
	v_mul_f32_e32 v92, v68, v60
	v_fmaak_f32 v60, v68, v60, 0x3b23d70a
	v_cmp_lt_f32_e32 vcc, v92, v75
	v_max_f32_e32 v70, 0xf149f2ca, v69
	s_nop 0
	v_cndmask_b32_e32 v60, 0, v60, vcc
	v_cmp_gt_f32_e32 vcc, v92, v73
	s_nop 1
	v_cndmask_b32_e32 v92, v60, v93, vcc
	v_max_f32_e32 v60, v70, v92
	v_cndmask_b32_e64 v60, v70, v60, s[0:1]
	v_mul_f32_e32 v70, v68, v71
	v_fmaak_f32 v93, v68, v71, 0xbb23d70a
	v_fmaak_f32 v71, v68, v71, 0x3b23d70a
	v_cmp_lt_f32_e32 vcc, v70, v75
	s_nop 1
	v_cndmask_b32_e32 v71, 0, v71, vcc
	v_cmp_gt_f32_e32 vcc, v70, v73
	s_nop 1
	v_cndmask_b32_e32 v70, v71, v93, vcc
	v_mul_f32_e32 v71, v68, v61
	v_fmaak_f32 v93, v68, v61, 0xbb23d70a
	v_fmaak_f32 v61, v68, v61, 0x3b23d70a
	v_cmp_lt_f32_e32 vcc, v71, v75
	v_max_f32_e32 v60, v60, v70
	s_nop 0
	v_cndmask_b32_e32 v61, 0, v61, vcc
	v_cmp_gt_f32_e32 vcc, v71, v73
	s_nop 1
	v_cndmask_b32_e32 v71, v61, v93, vcc
	v_max_f32_e32 v61, v60, v71
	v_cndmask_b32_e64 v60, v60, v61, s[0:1]
	v_mul_f32_e32 v61, v68, v72
	v_fmaak_f32 v93, v68, v72, 0xbb23d70a
	v_fmaak_f32 v72, v68, v72, 0x3b23d70a
	v_cmp_lt_f32_e32 vcc, v61, v75
	s_nop 1
	v_cndmask_b32_e32 v72, 0, v72, vcc
	v_cmp_gt_f32_e32 vcc, v61, v73
	v_mul_f32_e32 v61, v68, v62
	s_nop 0
	v_cndmask_b32_e32 v72, v72, v93, vcc
	v_fmaak_f32 v93, v68, v62, 0xbb23d70a
	v_fmaak_f32 v62, v68, v62, 0x3b23d70a
	v_cmp_lt_f32_e32 vcc, v61, v75
	v_max_f32_e32 v60, v60, v72
	s_nop 0
	v_cndmask_b32_e32 v62, 0, v62, vcc
	v_cmp_gt_f32_e32 vcc, v61, v73
	s_nop 1
	v_cndmask_b32_e32 v62, v62, v93, vcc
	v_max_f32_e32 v61, v60, v62
	v_cndmask_b32_e64 v60, v60, v61, s[0:1]
	v_mul_f32_e32 v61, v68, v59
	v_fmaak_f32 v93, v68, v59, 0xbb23d70a
	v_fmaak_f32 v59, v68, v59, 0x3b23d70a
	v_cmp_lt_f32_e32 vcc, v61, v75
	s_nop 1
	v_cndmask_b32_e32 v59, 0, v59, vcc
	v_cmp_gt_f32_e32 vcc, v61, v73
	s_nop 1
	v_cndmask_b32_e32 v93, v59, v93, vcc
	v_max_f32_e32 v59, v60, v93
	v_mul_f32_e32 v60, v68, v63
	v_cmp_gt_f32_e32 vcc, v60, v73
	v_fmac_f32_e32 v73, v68, v63
	v_cmp_lt_f32_e64 s[6:7], v60, v75
	v_fmac_f32_e32 v75, v68, v63
	s_nop 0
	v_cndmask_b32_e64 v60, 0, v73, s[6:7]
	v_cndmask_b32_e32 v63, v60, v75, vcc
	v_max_f32_e32 v60, v59, v63
	v_cndmask_b32_e64 v60, v59, v60, s[0:1]
	v_mov_b32_e32 v61, v60
	s_nop 1
	v_permlane16_swap_b32_e32 v60, v61
	v_max_f32_e32 v61, v60, v61
	v_mov_b32_e32 v74, v61
	s_nop 1
	v_permlane32_swap_b32_e32 v61, v74
	v_max_f32_e32 v74, v61, v74
	v_sub_f32_e32 v61, v69, v74
	v_mul_f32_e32 v61, 0x3fb8aa3b, v61
	v_exp_f32_e32 v69, v61
	v_sub_f32_e32 v61, v92, v74
	v_mul_f32_e32 v61, 0x3fb8aa3b, v61
	v_exp_f32_e32 v75, v61
	v_sub_f32_e32 v70, v70, v74
	v_sub_f32_e32 v71, v71, v74
	v_mul_f32_e32 v70, 0x3fb8aa3b, v70
	v_mul_f32_e32 v71, 0x3fb8aa3b, v71
	v_exp_f32_e32 v70, v70
	v_exp_f32_e32 v71, v71
	v_sub_f32_e32 v72, v72, v74
	v_sub_f32_e32 v62, v62, v74
	v_mul_f32_e32 v72, 0x3fb8aa3b, v72
	v_mul_f32_e32 v62, 0x3fb8aa3b, v62
	v_add_f32_e32 v73, 0, v69
	v_cndmask_b32_e64 v75, 0, v75, s[0:1]
	v_exp_f32_e32 v72, v72
	v_exp_f32_e32 v62, v62
	v_sub_f32_e32 v84, v93, v74
	v_sub_f32_e32 v63, v63, v74
	v_add_f32_e32 v73, v73, v75
	v_mul_f32_e32 v84, 0x3fb8aa3b, v84
	v_mul_f32_e32 v63, 0x3fb8aa3b, v63
	v_add_f32_e32 v73, v73, v70
	v_cndmask_b32_e64 v71, 0, v71, s[0:1]
	v_exp_f32_e32 v84, v84
	v_exp_f32_e32 v63, v63
	v_add_f32_e32 v73, v73, v71
	v_add_f32_e32 v73, v73, v72
	v_cndmask_b32_e64 v74, 0, v62, s[0:1]
	v_add_f32_e32 v62, v73, v74
	v_add_f32_e32 v62, v62, v84
	v_cndmask_b32_e64 v73, 0, v63, s[0:1]
	v_add_f32_e32 v85, v62, v73
	v_mov_b32_e32 v66, v85
	s_nop 1
	v_permlane16_swap_b32_e32 v85, v66
	v_add_f32_e32 v66, v85, v66
	v_mov_b32_e32 v67, v66
	s_nop 1
	v_permlane32_swap_b32_e32 v66, v67
	v_add_f32_e32 v66, v66, v67
	v_div_scale_f32 v67, s[6:7], v66, v66, 1.0
	v_rcp_f32_e32 v78, v67
	s_nop 0
	v_fma_f32 v68, -v67, v78, 1.0
	v_fmac_f32_e32 v78, v68, v78
	v_div_scale_f32 v68, vcc, 1.0, v66, 1.0
	v_mul_f32_e32 v77, v68, v78
	v_fma_f32 v79, -v67, v77, v68
	v_fmac_f32_e32 v77, v79, v78
	v_fma_f32 v67, -v67, v77, v68
	v_div_fmas_f32 v67, v67, v78, v77
	v_div_fixup_f32 v66, v67, v66, 1.0
	v_mov_b32_e32 v67, 0xbd4ccccd
	v_fmaak_f32 v68, v66, v69, 0xbd4ccccd
	v_fmaak_f32 v69, v66, v70, 0xbd4ccccd
	v_fmaak_f32 v70, v66, v72, 0xbd4ccccd
	v_fmaak_f32 v75, v66, v75, 0xbd4ccccd
	v_fmaak_f32 v71, v66, v71, 0xbd4ccccd
	v_fmaak_f32 v74, v66, v74, 0xbd4ccccd
	v_mul_f32_e32 v70, 0x4038aa3b, v70
	v_fmaak_f32 v72, v66, v84, 0xbd4ccccd
	v_mul_f32_e32 v75, 0x4038aa3b, v75
	v_mul_f32_e32 v71, 0x4038aa3b, v71
	v_mul_f32_e32 v74, 0x4038aa3b, v74
	v_fmac_f32_e32 v67, v66, v73
	v_mul_f32_e32 v68, 0x4038aa3b, v68
	v_mul_f32_e32 v69, 0x4038aa3b, v69
	v_mul_f32_e32 v72, 0x4038aa3b, v72
	v_cndmask_b32_e64 v75, 0, v75, s[0:1]
	v_cndmask_b32_e64 v71, 0, v71, s[0:1]
	v_cndmask_b32_e64 v74, 0, v74, s[0:1]
	v_mul_f32_e32 v66, 0x4038aa3b, v67
	v_cvt_pk_bf16_f32 v67, v70, v72
	v_add_u32_e32 v70, v76, v198
	v_cndmask_b32_e64 v73, 0, v66, s[0:1]
	v_cndmask_b32_e64 v74, v74, 1.0, s[4:5]
	v_cndmask_b32_e64 v75, v75, 1.0, s[4:5]
	v_cndmask_b32_e64 v71, v71, 1.0, s[4:5]
	v_cvt_pk_bf16_f32 v66, v68, v69
	v_cvt_pk_bf16_f32 v68, v75, v71
	v_cvt_pk_bf16_f32 v69, v74, v73
	ds_write_b128 v70, v[66:69]
	s_movk_i32 s0, 0x210
	v_and_b32_e32 v67, 48, v0
	v_lshrrev_b32_e32 v0, 5, v1
	v_mad_u32_u24 v66, v197, s0, v199
	v_mad_u32_u24 v68, v0, s0, v199
	s_and_b32 s0, s2, 7
	s_lshl_b32 s0, s0, 22
	s_lshl_b32 s1, s3, 17
	v_lshlrev_b32_e32 v1, 13, v0
	s_add_i32 s0, s0, s1
	v_and_b32_e32 v69, 0x1f0, v194
	v_or3_b32 v1, s0, v1, v196
	s_mov_b32 s12, 0
	s_mov_b32 s11, 0x20000
	s_brev_b32 s10, 8
	s_and_b32 s9, s9, 0xffff
	v_or_b32_e32 v0, 0x24800, v198
	v_add_u32_e32 v1, v1, v69
	v_add_u32_e32 v106, v66, v67
	v_add_u32_e32 v107, v68, v69
	s_waitcnt lgkmcnt(0)
	s_barrier
